# speedup vs baseline: 1.0493x; 1.0006x over previous
_Z11lstm_kernelPKiPKhPKfS4_S4_Pf:
	s_load_dwordx4 s[12:15], s[0:1], 0x0
	v_readfirstlane_b32 s19, v0
	v_or_b32_e32 v3, 0x400, v0
	s_movk_i32 s4, 0x500
	s_lshr_b32 s7, s19, 6
	s_lshl_b32 s18, s2, 6
	s_mulk_i32 s2, 0x1400
	v_mov_b32_e32 v2, 0x4ff
	v_cmp_gt_u32_e32 vcc, s4, v3
	s_mul_hi_i32 s3, s18, 0x50
	s_waitcnt lgkmcnt(0)
	s_add_u32 s2, s12, s2
	v_cndmask_b32_e32 v2, v2, v3, vcc
	s_addc_u32 s3, s13, s3
	v_lshlrev_b32_e32 v1, 2, v0
	v_lshlrev_b32_e32 v4, 2, v2
	s_movk_i32 s4, 0x184
	v_or_b32_e32 v28, 0x200, v0
	global_load_dword v29, v1, s[2:3]
	global_load_dword v30, v1, s[2:3] offset:2048
	global_load_dword v2, v4, s[2:3]
	v_mov_b32_e32 v4, 0x383
	v_cmp_gt_u32_e32 vcc, s4, v0
	s_add_u32 s2, s14, 0x34000
	s_addc_u32 s3, s15, 0
	v_cndmask_b32_e32 v4, v4, v28, vcc
	v_lshlrev_b32_e32 v31, 4, v0
	v_lshlrev_b32_e32 v4, 4, v4
	global_load_dwordx4 v[6:9], v31, s[2:3]
	global_load_dwordx4 v[10:13], v4, s[2:3]
	v_and_b32_e32 v4, 0x7f, v0
	v_lshlrev_b32_e32 v18, 4, v4
	v_mov_b32_e32 v19, 0
	v_lshl_add_u64 v[4:5], s[14:15], 0, v[18:19]
	s_mov_b32 s2, 0x37000
	v_add_co_u32_e64 v4, s[2:3], s2, v4
	s_nop 1
	v_addc_co_u32_e64 v5, s[2:3], 0, v5, s[2:3]
	global_load_dwordx4 v[14:17], v[4:5], off offset:2112
	s_movk_i32 s22, 0x410
	s_movk_i32 s2, 0x4ff
	v_and_b32_e32 v4, 63, v0
	v_cmp_lt_u32_e64 s[2:3], s2, v3
	s_mul_i32 s5, s7, 0x6000
	s_mul_hi_u32 s4, s7, 0x6000
	s_add_u32 s8, s14, s5
	s_addc_u32 s9, s15, s4
	v_lshlrev_b32_e32 v210, 4, v4
	v_mov_b32_e32 v211, v19
	v_lshl_add_u64 v[20:21], s[8:9], 0, v[210:211]
	s_movk_i32 s4, 0x2000
	v_add_co_u32_e64 v22, s[4:5], s4, v20
	s_nop 1
	v_addc_co_u32_e64 v23, s[4:5], 0, v21, s[4:5]
	s_movk_i32 s4, 0x3000
	s_nop 0
	v_add_co_u32_e64 v24, s[4:5], s4, v20
	global_load_dwordx4 v[90:93], v[22:23], off offset:1024
	global_load_dwordx4 v[86:89], v[22:23], off offset:2048
	v_addc_co_u32_e64 v25, s[4:5], 0, v21, s[4:5]
	s_movk_i32 s4, 0x5000
	s_nop 0
	v_add_co_u32_e64 v26, s[4:5], s4, v20
	s_nop 1
	v_addc_co_u32_e64 v27, s[4:5], 0, v21, s[4:5]
	global_load_dwordx4 v[82:85], v[22:23], off offset:3072
	global_load_dwordx4 v[46:49], v[26:27], off
	global_load_dwordx4 v[42:45], v[26:27], off offset:1024
	global_load_dwordx4 v[38:41], v[26:27], off offset:2048
	global_load_dwordx4 v[94:97], v[24:25], off offset:-4096
	global_load_dwordx4 v[34:37], v[26:27], off offset:3072
	s_movk_i32 s4, 0x1000
	v_add_co_u32_e64 v22, s[4:5], s4, v20
	global_load_dwordx4 v[126:129], v210, s[8:9]
	global_load_dwordx4 v[122:125], v210, s[8:9] offset:1024
	global_load_dwordx4 v[118:121], v210, s[8:9] offset:2048
	global_load_dwordx4 v[114:117], v210, s[8:9] offset:3072
	v_addc_co_u32_e64 v23, s[4:5], 0, v21, s[4:5]
	global_load_dwordx4 v[110:113], v[22:23], off
	global_load_dwordx4 v[106:109], v[22:23], off offset:1024
	global_load_dwordx4 v[102:105], v[22:23], off offset:2048
	global_load_dwordx4 v[98:101], v[22:23], off offset:3072
	global_load_dwordx4 v[78:81], v[24:25], off
	global_load_dwordx4 v[74:77], v[24:25], off offset:1024
	global_load_dwordx4 v[70:73], v[24:25], off offset:2048
	global_load_dwordx4 v[66:69], v[24:25], off offset:3072
	s_movk_i32 s4, 0x4000
	v_add_co_u32_e64 v20, s[4:5], s4, v20
	v_mov_b32_e32 v5, 0x4000
	s_nop 0
	v_addc_co_u32_e64 v21, s[4:5], 0, v21, s[4:5]
	global_load_dwordx4 v[62:65], v[20:21], off
	global_load_dwordx4 v[58:61], v[20:21], off offset:1024
	global_load_dwordx4 v[54:57], v[20:21], off offset:2048
	global_load_dwordx4 v[50:53], v[20:21], off offset:3072
	s_waitcnt vmcnt(26)
	ds_write_b128 v31, v[6:9] offset:16384
	v_lshl_or_b32 v5, v28, 4, v5
	v_add_u32_e32 v6, 0x9840, v31
	v_cndmask_b32_e32 v5, v6, v5, vcc
	s_waitcnt vmcnt(25)
	ds_write_b128 v5, v[10:13]
	s_waitcnt vmcnt(24)
	ds_write_b128 v18, v[14:17] offset:36928
	v_mul_u32_u24_e32 v5, 0xccd, v0
	v_lshrrev_b32_e32 v5, 16, v5
	s_mov_b32 s5, 0xffffec
	v_mul_u32_u24_e32 v6, 0xccd, v28
	s_movk_i32 s4, 0x90
	v_mad_u32_u24 v8, v5, s5, v0
	v_lshlrev_b32_e32 v5, 2, v5
	v_lshrrev_b32_e32 v6, 16, v6
	v_mul_lo_u32 v7, v29, s4
	v_lshl_or_b32 v5, v8, 8, v5
	ds_write_b32 v5, v7 offset:30784
	v_mul_lo_u32 v196, v29, s22
	v_add_u32_e32 v197, 0x24e80, v5
	ds_write_b32 v197, v196
	v_mad_u32_u24 v7, v6, s5, v28
	v_lshlrev_b32_e32 v6, 2, v6
	v_mul_lo_u32 v5, v30, s4
	v_lshl_or_b32 v6, v7, 8, v6
	ds_write_b32 v6, v5 offset:30784
	v_mul_lo_u32 v198, v30, s22
	v_add_u32_e32 v199, 0x24e80, v6
	ds_write_b32 v199, v198
	s_and_saveexec_b64 s[4:5], s[2:3]
	s_xor_b64 s[2:3], exec, s[4:5]
	v_mov_b32_e32 v3, 0x9840
	v_lshl_add_u32 v5, v0, 2, v3
	s_andn2_saveexec_b64 s[2:3], s[2:3]
	v_mul_u32_u24_e32 v5, 0xccd, v3
	s_mov_b32 s4, 0xffffec
	v_mul_u32_u24_sdwa v6, v5, s4 dst_sel:DWORD dst_unused:UNUSED_PAD src0_sel:WORD_1 src1_sel:DWORD
	v_add_lshl_u32 v3, v6, v3, 8
	v_mov_b32_e32 v6, 2
	v_lshlrev_b32_sdwa v5, v6, v5 dst_sel:DWORD dst_unused:UNUSED_PAD src0_sel:DWORD src1_sel:WORD_1
	s_movk_i32 s4, 0x7840
	v_add3_u32 v5, v5, v3, s4
	s_or_b64 exec, exec, s[2:3]
	v_lshrrev_b32_e32 v3, 5, v4
	s_movk_i32 s2, 0x90
	s_lshl_b32 s6, s7, 10
	s_mulk_i32 s7, 0xfd00
	v_and_b32_e32 v182, 31, v0
	v_mul_lo_u32 v200, v2, s22
	v_mul_lo_u32 v2, v2, s2
	s_add_i32 s7, s6, s7
	v_lshlrev_b32_e32 v229, 6, v3
	ds_write_b32 v5, v2
	v_add_u32_e32 v201, 0x1d640, v5
	ds_write_b32 v201, v200
	v_lshlrev_b32_e32 v230, 4, v3
	v_lshlrev_b32_e32 v228, 2, v182
	v_or_b32_e32 v2, s7, v229
	v_mov_b32_e32 v204, 0
	v_mov_b32_e32 v205, 0
	v_mov_b32_e32 v206, 0
	v_mov_b32_e32 v207, 0
	ds_write_b128 v31, v[204:207]
	ds_write_b128 v31, v[204:207] offset:8192
	v_and_b32_e32 v202, 0xfc, v1
	v_add_u32_e32 v202, 0x26280, v202
	ds_write_b32 v202, v204
	s_waitcnt lgkmcnt(0)
	s_barrier
	s_cmpk_lt_u32 s19, 0x100
	s_cbranch_scc1 .Llight_path
	s_setprio 1
	v_add_u32_e32 v3, 0x7800, v228
	ds_read2_b32 v[138:139], v3 offset0:16 offset1:48
	ds_read_b128 v[18:21], v2 offset:36928
	ds_read_b128 v[22:25], v2 offset:36944
	s_waitcnt lgkmcnt(2)
	v_add_u32_e32 v3, v230, v138
	ds_read_b128 v[26:29], v2 offset:36960
	ds_read_b128 v[30:33], v2 offset:36976
	ds_read_b128 v[142:145], v3 offset:16384
	ds_read_b128 v[130:133], v3 offset:16416
	ds_read_b128 v[154:157], v3 offset:16448
	ds_read_b128 v[134:137], v3 offset:16480
	ds_read_b128 v[248:251], v2 offset:37104
	ds_read_b128 v[244:247], v2 offset:37088
	ds_read_b128 v[240:243], v2 offset:37072
	ds_read_b128 v[236:239], v2 offset:37056
	s_waitcnt vmcnt(17) lgkmcnt(7)
	v_mfma_f32_32x32x16_bf16 v[18:33], v[94:97], v[142:145], v[18:33]
	s_waitcnt lgkmcnt(6)
	v_mfma_f32_32x32x16_bf16 v[18:33], v[90:93], v[130:133], v[18:33]
	s_waitcnt lgkmcnt(5)
	v_mfma_f32_32x32x16_bf16 v[18:33], v[86:89], v[154:157], v[18:33]
	s_waitcnt lgkmcnt(4)
	v_mfma_f32_32x32x16_bf16 v[18:33], v[82:85], v[134:137], v[18:33]
	s_cmpk_lt_u32 s19, 0x100
	s_cselect_b64 s[2:3], -1, 0
	ds_read_b32 v158, v228 offset:31040
	v_add_u32_e32 v159, v230, v139
	s_nop 2
	v_exp_f32_e32 v139, v20
	v_exp_f32_e32 v138, v24
	v_exp_f32_e32 v141, v28
	v_exp_f32_e32 v140, v32
	v_exp_f32_e32 v18, v18
	v_exp_f32_e32 v20, v22
	v_exp_f32_e32 v22, v26
	v_add_f32_e32 v24, 1.0, v138
	v_add_f32_e32 v26, 1.0, v141
	v_add_f32_e32 v19, 1.0, v139
	v_exp_f32_e32 v23, v30
	v_add_f32_e32 v27, 1.0, v140
	v_fmac_f32_e32 v24, v20, v24
	v_fmac_f32_e32 v26, v22, v26
	v_fmac_f32_e32 v19, v18, v19
	v_fmac_f32_e32 v27, v23, v27
	v_rcp_f32_e32 v18, v24
	v_rcp_f32_e32 v22, v27
	v_rcp_f32_e32 v19, v19
	v_rcp_f32_e32 v23, v26
	v_exp_f32_e32 v146, v21
	v_exp_f32_e32 v147, v25
	s_mov_b32 s8, 0xc038aa3b
	s_mov_b32 s4, 0x4038aa3b
	v_mov_b64_e32 v[160:161], s[8:9]
	v_exp_f32_e32 v148, v29
	v_exp_f32_e32 v149, v33
	v_pk_fma_f32 v[20:21], v[138:139], s[4:5], v[160:161] op_sel_hi:[1,0,0]
	s_nop 0
	v_pk_mul_f32 v[214:215], v[20:21], v[18:19]
	v_pk_fma_f32 v[18:19], v[140:141], s[4:5], v[160:161] op_sel_hi:[1,0,0]
	s_nop 0
	v_pk_mul_f32 v[212:213], v[18:19], v[22:23]
	v_add_u32_e32 v231, s7, v229
	ds_read_b128 v[18:21], v231 offset:36928
	ds_read_b128 v[22:25], v231 offset:36944
	ds_read_b128 v[26:29], v231 offset:36960
	ds_read_b128 v[30:33], v231 offset:36976
	s_waitcnt lgkmcnt(5)
	v_mfma_f32_32x32x16_bf16 v[2:17], v[46:49], v[142:145], v[236:251]
	ds_read_b128 v[138:141], v159 offset:16384
	v_add_f32_e32 v162, 1.0, v146
	v_exp_f32_e32 v163, v215
	v_exp_f32_e32 v164, v214
	v_exp_f32_e32 v165, v213
	v_exp_f32_e32 v166, v212
	v_add_f32_e32 v142, 1.0, v147
	v_add_f32_e32 v143, 1.0, v148
	v_add_f32_e32 v144, 1.0, v149
	v_mfma_f32_32x32x16_bf16 v[2:17], v[42:45], v[130:133], v[2:17]
	ds_read_b128 v[146:149], v159 offset:16416
	v_fmac_f32_e32 v162, v162, v163
	v_fmac_f32_e32 v142, v142, v164
	v_fmac_f32_e32 v143, v143, v165
	v_fmac_f32_e32 v144, v144, v166
	v_mfma_f32_32x32x16_bf16 v[2:17], v[38:41], v[154:157], v[2:17]
	ds_read_b128 v[150:153], v159 offset:16448
	v_rcp_f32_e32 v130, v162
	v_rcp_f32_e32 v131, v142
	v_rcp_f32_e32 v132, v143
	v_rcp_f32_e32 v133, v144
	s_waitcnt vmcnt(16)
	v_mfma_f32_32x32x16_bf16 v[2:17], v[34:37], v[134:137], v[2:17]
	ds_read_b128 v[178:181], v159 offset:16480
	v_fma_f32 v130, -v163, v130, v130
	v_fma_f32 v131, -v164, v131, v131
	v_fma_f32 v132, -v165, v132, v132
	v_fma_f32 v133, -v166, v133, v133
	v_add_u32_e32 v211, s6, v210
	v_cvt_pk_bf16_f32 v130, v130, v131
	v_cvt_pk_bf16_f32 v131, v132, v133
	ds_write_b64 v211, v[130:131]
	s_nop 3
	v_exp_f32_e32 v131, v4
	v_exp_f32_e32 v130, v8
	v_exp_f32_e32 v133, v12
	v_exp_f32_e32 v132, v16
	v_exp_f32_e32 v2, v2
	v_exp_f32_e32 v4, v6
	v_exp_f32_e32 v6, v10
	v_exp_f32_e32 v7, v14
	v_add_f32_e32 v3, 1.0, v131
	v_add_f32_e32 v8, 1.0, v130
	v_add_f32_e32 v10, 1.0, v133
	v_add_f32_e32 v11, 1.0, v132
	v_fmac_f32_e32 v3, v2, v3
	v_fmac_f32_e32 v8, v4, v8
	v_fmac_f32_e32 v10, v6, v10
	v_fmac_f32_e32 v11, v7, v11
	v_rcp_f32_e32 v3, v3
	v_rcp_f32_e32 v2, v8
	v_rcp_f32_e32 v7, v10
	v_rcp_f32_e32 v6, v11
	v_exp_f32_e32 v134, v5
	v_exp_f32_e32 v135, v9
	v_pk_fma_f32 v[4:5], v[130:131], s[4:5], v[160:161] op_sel_hi:[1,0,0]
	v_exp_f32_e32 v130, v13
	v_pk_mul_f32 v[204:205], v[4:5], v[2:3]
	v_pk_fma_f32 v[2:3], v[132:133], s[4:5], v[160:161] op_sel_hi:[1,0,0]
	v_exp_f32_e32 v131, v17
	v_pk_mul_f32 v[202:203], v[2:3], v[6:7]
	s_waitcnt lgkmcnt(4)
	v_mfma_f32_32x32x16_bf16 v[18:33], v[94:97], v[138:141], v[18:33]
	v_add_f32_e32 v132, 1.0, v134
	v_exp_f32_e32 v133, v205
	v_add_f32_e32 v134, 1.0, v135
	v_exp_f32_e32 v135, v204
	v_exp_f32_e32 v136, v203
	v_exp_f32_e32 v137, v202
	v_add_f32_e32 v130, 1.0, v130
	v_add_f32_e32 v131, 1.0, v131
	s_waitcnt lgkmcnt(3)
	v_mfma_f32_32x32x16_bf16 v[18:33], v[90:93], v[146:149], v[18:33]
	v_fmac_f32_e32 v132, v132, v133
	v_fmac_f32_e32 v134, v134, v135
	v_fmac_f32_e32 v130, v130, v136
	v_fmac_f32_e32 v131, v131, v137
	s_waitcnt lgkmcnt(2)
	v_mfma_f32_32x32x16_bf16 v[18:33], v[86:89], v[150:153], v[18:33]
	v_rcp_f32_e32 v132, v132
	v_rcp_f32_e32 v134, v134
	v_rcp_f32_e32 v130, v130
	v_rcp_f32_e32 v131, v131
	s_waitcnt lgkmcnt(1)
	v_mfma_f32_32x32x16_bf16 v[18:33], v[82:85], v[178:181], v[18:33]
	v_fma_f32 v132, -v133, v132, v132
	v_fma_f32 v133, -v135, v134, v134
	v_fma_f32 v134, -v136, v130, v130
	v_fma_f32 v131, -v137, v131, v131
	v_cvt_pk_bf16_f32 v130, v132, v133
	v_cvt_pk_bf16_f32 v131, v134, v131
	ds_write_b64 v211, v[130:131] offset:8
	s_waitcnt lgkmcnt(0)
	s_barrier
	s_load_dwordx8 s[4:11], s[0:1], 0x10
	ds_read_b32 v194, v228 offset:31168
	ds_read_b128 v[174:177], v210
	v_add_u32_e32 v183, v230, v158
	ds_read_b128 v[170:173], v210 offset:1024
	v_exp_f32_e32 v131, v20
	v_exp_f32_e32 v130, v24
	v_exp_f32_e32 v133, v28
	v_exp_f32_e32 v132, v32
	ds_read_b128 v[166:169], v210 offset:2048
	v_exp_f32_e32 v18, v18
	v_exp_f32_e32 v20, v22
	v_exp_f32_e32 v22, v26
	v_exp_f32_e32 v23, v30
	v_add_f32_e32 v19, 1.0, v131
	v_add_f32_e32 v24, 1.0, v130
	v_add_f32_e32 v26, 1.0, v133
	v_add_f32_e32 v27, 1.0, v132
	ds_read_b128 v[162:165], v210 offset:3072
	v_fmac_f32_e32 v19, v18, v19
	v_fmac_f32_e32 v24, v20, v24
	v_fmac_f32_e32 v26, v22, v26
	v_fmac_f32_e32 v27, v23, v27
	ds_read_b128 v[158:161], v210 offset:4096
	v_rcp_f32_e32 v19, v19
	v_rcp_f32_e32 v18, v24
	v_rcp_f32_e32 v23, v26
	v_rcp_f32_e32 v22, v27
	ds_read_b128 v[154:157], v210 offset:5120
	v_exp_f32_e32 v186, v21
	v_exp_f32_e32 v187, v25
	ds_read_b128 v[142:145], v210 offset:6144
	s_mov_b32 s0, 0xc038aa3b
	s_mov_b32 s12, 0x4038aa3b
	v_mov_b64_e32 v[184:185], s[0:1]
	v_pk_fma_f32 v[20:21], v[130:131], s[12:13], v[184:185] op_sel_hi:[1,0,0]
	v_exp_f32_e32 v188, v29
	v_pk_mul_f32 v[200:201], v[20:21], v[18:19]
	v_pk_fma_f32 v[18:19], v[132:133], s[12:13], v[184:185] op_sel_hi:[1,0,0]
	v_exp_f32_e32 v189, v33
	v_pk_mul_f32 v[198:199], v[18:19], v[22:23]
	ds_read_b128 v[130:133], v210 offset:7168
	ds_read_b128 v[18:21], v231 offset:36928
	ds_read_b128 v[22:25], v231 offset:36944
	ds_read_b128 v[26:29], v231 offset:36960
	ds_read_b128 v[30:33], v231 offset:36976
	v_mfma_f32_32x32x16_bf16 v[2:17], v[46:49], v[138:141], v[236:251]
	ds_read_b128 v[134:137], v183 offset:16384
	v_add_f32_e32 v186, 1.0, v186
	v_exp_f32_e32 v190, v201
	v_exp_f32_e32 v191, v200
	v_exp_f32_e32 v192, v199
	v_exp_f32_e32 v193, v198
	v_add_f32_e32 v187, 1.0, v187
	v_add_f32_e32 v188, 1.0, v188
	v_add_f32_e32 v189, 1.0, v189
	v_mfma_f32_32x32x16_bf16 v[2:17], v[42:45], v[146:149], v[2:17]
	ds_read_b128 v[138:141], v183 offset:16416
	v_fmac_f32_e32 v186, v186, v190
	v_fmac_f32_e32 v187, v187, v191
	v_fmac_f32_e32 v188, v188, v192
	v_fmac_f32_e32 v189, v189, v193
	v_mfma_f32_32x32x16_bf16 v[2:17], v[38:41], v[150:153], v[2:17]
	ds_read_b128 v[146:149], v183 offset:16448
	v_rcp_f32_e32 v186, v186
	v_rcp_f32_e32 v187, v187
	v_rcp_f32_e32 v188, v188
	v_rcp_f32_e32 v189, v189
	v_mfma_f32_32x32x16_bf16 v[2:17], v[34:37], v[178:181], v[2:17]
	ds_read_b128 v[150:153], v183 offset:16480
	v_fma_f32 v183, -v190, v186, v186
	v_fma_f32 v186, -v191, v187, v187
	v_fma_f32 v187, -v192, v188, v188
	v_fma_f32 v188, -v193, v189, v189
	s_waitcnt vmcnt(15) lgkmcnt(0)
	v_mfma_f32_32x32x16_bf16 v[18:33], v[126:129], v[174:177], v[18:33]
	v_cvt_pk_bf16_f32 v178, v183, v186
	v_cvt_pk_bf16_f32 v179, v187, v188
	ds_write_b64 v211, v[178:179] offset:8192
	s_waitcnt vmcnt(14)
	v_mfma_f32_32x32x16_bf16 v[18:33], v[122:125], v[170:173], v[18:33]
	s_nop 0
	v_exp_f32_e32 v179, v4
	v_exp_f32_e32 v178, v8
	v_exp_f32_e32 v181, v12
	v_exp_f32_e32 v180, v16
	s_waitcnt vmcnt(13)
	v_mfma_f32_32x32x16_bf16 v[18:33], v[118:121], v[166:169], v[18:33]
	v_exp_f32_e32 v2, v2
	v_exp_f32_e32 v4, v6
	v_exp_f32_e32 v7, v10
	v_exp_f32_e32 v8, v14
	v_add_f32_e32 v3, 1.0, v179
	v_add_f32_e32 v6, 1.0, v178
	v_add_f32_e32 v10, 1.0, v181
	v_add_f32_e32 v11, 1.0, v180
	s_waitcnt vmcnt(12)
	v_mfma_f32_32x32x16_bf16 v[18:33], v[114:117], v[162:165], v[18:33]
	v_fmac_f32_e32 v3, v2, v3
	v_fmac_f32_e32 v6, v4, v6
	v_fmac_f32_e32 v10, v7, v10
	v_fmac_f32_e32 v11, v8, v11
	s_waitcnt vmcnt(11)
	v_mfma_f32_32x32x16_bf16 v[18:33], v[110:113], v[158:161], v[18:33]
	v_rcp_f32_e32 v3, v3
	v_rcp_f32_e32 v2, v6
	v_rcp_f32_e32 v7, v10
	v_rcp_f32_e32 v6, v11
	s_waitcnt vmcnt(10)
	v_mfma_f32_32x32x16_bf16 v[18:33], v[106:109], v[154:157], v[18:33]
	v_exp_f32_e32 v183, v5
	v_exp_f32_e32 v186, v9
	s_waitcnt vmcnt(9)
	v_mfma_f32_32x32x16_bf16 v[18:33], v[102:105], v[142:145], v[18:33]
	v_fma_f32 v4, v178, s12, v184
	v_fma_f32 v5, v179, s12, v184
	v_exp_f32_e32 v178, v13
	v_pk_mul_f32 v[206:207], v[4:5], v[2:3]
	v_pk_fma_f32 v[2:3], v[180:181], s[12:13], v[184:185] op_sel_hi:[1,0,0]
	v_exp_f32_e32 v179, v17
	v_pk_mul_f32 v[208:209], v[2:3], v[6:7]
	s_waitcnt vmcnt(8)
	v_mfma_f32_32x32x16_bf16 v[18:33], v[98:101], v[130:133], v[18:33]
	v_mfma_f32_32x32x16_bf16 v[18:33], v[94:97], v[134:137], v[18:33]
	v_add_f32_e32 v180, 1.0, v183
	v_exp_f32_e32 v181, v207
	v_add_f32_e32 v183, 1.0, v186
	v_exp_f32_e32 v184, v206
	v_exp_f32_e32 v185, v209
	v_exp_f32_e32 v186, v208
	v_add_f32_e32 v178, 1.0, v178
	v_add_f32_e32 v179, 1.0, v179
	v_mfma_f32_32x32x16_bf16 v[18:33], v[90:93], v[138:141], v[18:33]
	v_fmac_f32_e32 v180, v180, v181
	v_fmac_f32_e32 v183, v183, v184
	v_fmac_f32_e32 v178, v178, v185
	v_fmac_f32_e32 v179, v179, v186
	v_mfma_f32_32x32x16_bf16 v[18:33], v[86:89], v[146:149], v[18:33]
	v_rcp_f32_e32 v180, v180
	v_rcp_f32_e32 v183, v183
	v_rcp_f32_e32 v178, v178
	v_rcp_f32_e32 v179, v179
	v_mfma_f32_32x32x16_bf16 v[18:33], v[82:85], v[150:153], v[18:33]
	v_fma_f32 v180, -v181, v180, v180
	v_fma_f32 v181, -v184, v183, v183
	v_fma_f32 v183, -v185, v178, v178
	v_fma_f32 v179, -v186, v179, v179
	v_cvt_pk_bf16_f32 v178, v180, v181
	v_cvt_pk_bf16_f32 v179, v183, v179
	ds_write_b64 v211, v[178:179] offset:8200
	s_waitcnt lgkmcnt(0)
	s_barrier
	v_mov_b32_e32 v178, 0x7a40
	v_lshl_add_u32 v232, v182, 2, v178
	s_mov_b32 s1, -1
	s_branch .LBB1_14
.LBB1_13:
	v_mfma_f32_32x32x16_bf16 v[2:17], v[78:81], v[206:209], v[236:251]
	ds_read_b32 v194, v232 offset:384
	ds_read_b128 v[174:177], v210
	v_add_u32_e32 v195, v230, v233
	v_mfma_f32_32x32x16_bf16 v[2:17], v[74:77], v[190:193], v[2:17]
	ds_read_b128 v[170:173], v210 offset:1024
	v_exp_f32_e32 v199, v28
	v_exp_f32_e32 v198, v32
	v_exp_f32_e32 v197, v20
	v_exp_f32_e32 v196, v24
	v_mfma_f32_32x32x16_bf16 v[2:17], v[70:73], v[158:161], v[2:17]
	ds_read_b128 v[166:169], v210 offset:2048
	v_exp_f32_e32 v18, v18
	v_exp_f32_e32 v22, v22
	v_exp_f32_e32 v24, v26
	v_exp_f32_e32 v26, v30
	v_add_f32_e32 v20, 1.0, v197
	v_add_f32_e32 v28, 1.0, v196
	v_add_f32_e32 v30, 1.0, v199
	v_add_f32_e32 v32, 1.0, v198
	v_mfma_f32_32x32x16_bf16 v[2:17], v[66:69], v[142:145], v[2:17]
	ds_read_b128 v[162:165], v210 offset:3072
	v_exp_f32_e32 v19, v19
	v_exp_f32_e32 v23, v23
	v_exp_f32_e32 v27, v27
	v_exp_f32_e32 v31, v31
	v_fmac_f32_e32 v20, v18, v20
	v_fmac_f32_e32 v28, v22, v28
	v_fmac_f32_e32 v30, v24, v30
	v_fmac_f32_e32 v32, v26, v32
	v_mfma_f32_32x32x16_bf16 v[2:17], v[62:65], v[154:157], v[2:17]
	ds_read_b128 v[158:161], v210 offset:4096
	v_add_f32_e32 v22, 1.0, v19
	v_rcp_f32_e32 v19, v20
	v_rcp_f32_e32 v18, v28
	v_add_f32_e32 v20, 1.0, v23
	v_rcp_f32_e32 v191, v30
	v_rcp_f32_e32 v190, v32
	v_mfma_f32_32x32x16_bf16 v[2:17], v[58:61], v[182:185], v[2:17]
	ds_read_b128 v[154:157], v210 offset:5120
	v_exp_f32_e32 v206, v21
	v_exp_f32_e32 v207, v25
	v_add_f32_e32 v23, 1.0, v27
	v_rcp_f32_e32 v192, v20
	v_add_f32_e32 v20, 1.0, v31
	v_rcp_f32_e32 v193, v22
	v_mfma_f32_32x32x16_bf16 v[2:17], v[54:57], v[186:189], v[2:17]
	ds_read_b128 v[142:145], v210 offset:6144
	v_exp_f32_e32 v208, v29
	v_exp_f32_e32 v209, v33
	v_rcp_f32_e32 v183, v23
	v_rcp_f32_e32 v182, v20
	v_mfma_f32_32x32x16_bf16 v[2:17], v[50:53], v[134:137], v[2:17]
	v_mov_b64_e32 v[184:185], s[0:1]
	v_fma_f32 v20, v196, s12, v184
	v_fma_f32 v21, v197, s12, v184
	ds_read_b128 v[130:133], v210 offset:7168
	v_mul_f32_e64 v186, v20, v18
	v_mul_f32_e64 v187, v21, v19
	ds_read_b128 v[18:21], v231 offset:36928
	ds_read_b128 v[22:25], v231 offset:36944
	ds_read_b128 v[26:29], v231 offset:36960
	ds_read_b128 v[30:33], v231 offset:36976
	v_pk_fma_f32 v[134:135], v[198:199], s[12:13], v[184:185] op_sel_hi:[1,0,0]
	v_pk_fma_f32 v[200:201], v[192:193], v[220:221], v[186:187]
	v_pk_mul_f32 v[134:135], v[134:135], v[190:191]
	s_nop 0
	v_pk_fma_f32 v[198:199], v[182:183], v[222:223], v[134:135]
	v_mfma_f32_32x32x16_bf16 v[2:17], v[46:49], v[138:141], v[2:17]
	ds_read_b128 v[134:137], v195 offset:16384
	v_add_f32_e32 v182, 1.0, v206
	v_exp_f32_e32 v183, v201
	v_exp_f32_e32 v186, v200
	v_exp_f32_e32 v187, v199
	v_exp_f32_e32 v188, v198
	v_add_f32_e32 v189, 1.0, v207
	v_add_f32_e32 v190, 1.0, v208
	v_add_f32_e32 v191, 1.0, v209
	v_mfma_f32_32x32x16_bf16 v[2:17], v[42:45], v[146:149], v[2:17]
	ds_read_b128 v[138:141], v195 offset:16416
	v_fmac_f32_e32 v182, v182, v183
	v_fmac_f32_e32 v189, v189, v186
	v_fmac_f32_e32 v190, v190, v187
	v_fmac_f32_e32 v191, v191, v188
	v_mfma_f32_32x32x16_bf16 v[2:17], v[38:41], v[150:153], v[2:17]
	ds_read_b128 v[146:149], v195 offset:16448
	v_rcp_f32_e32 v182, v182
	v_rcp_f32_e32 v189, v189
	v_rcp_f32_e32 v190, v190
	v_rcp_f32_e32 v191, v191
	v_mfma_f32_32x32x16_bf16 v[2:17], v[34:37], v[178:181], v[2:17]
	ds_read_b128 v[150:153], v195 offset:16480
	v_fma_f32 v182, -v183, v182, v182
	v_fma_f32 v183, -v186, v189, v189
	v_fma_f32 v186, -v187, v190, v190
	v_fma_f32 v187, -v188, v191, v191
	s_waitcnt lgkmcnt(4)
	v_mfma_f32_32x32x16_bf16 v[18:33], v[126:129], v[174:177], v[18:33]
	v_cvt_pk_bf16_f32 v178, v182, v183
	v_cvt_pk_bf16_f32 v179, v186, v187
	ds_write_b64 v211, v[178:179] offset:8192
	v_mfma_f32_32x32x16_bf16 v[18:33], v[122:125], v[170:173], v[18:33]
	s_nop 1
	v_exp_f32_e32 v179, v4
	v_exp_f32_e32 v178, v8
	v_exp_f32_e32 v181, v12
	v_exp_f32_e32 v180, v16
	v_mfma_f32_32x32x16_bf16 v[18:33], v[118:121], v[166:169], v[18:33]
	v_exp_f32_e32 v2, v2
	v_exp_f32_e32 v6, v6
	v_exp_f32_e32 v10, v10
	v_exp_f32_e32 v12, v14
	v_add_f32_e32 v4, 1.0, v179
	v_add_f32_e32 v8, 1.0, v178
	v_add_f32_e32 v14, 1.0, v181
	v_add_f32_e32 v16, 1.0, v180
	v_mfma_f32_32x32x16_bf16 v[18:33], v[114:117], v[162:165], v[18:33]
	v_exp_f32_e32 v3, v3
	v_fmac_f32_e32 v4, v2, v4
	v_exp_f32_e32 v2, v7
	v_fmac_f32_e32 v8, v6, v8
	v_exp_f32_e32 v6, v11
	v_exp_f32_e32 v7, v15
	v_fmac_f32_e32 v14, v10, v14
	v_fmac_f32_e32 v16, v12, v16
	v_mfma_f32_32x32x16_bf16 v[18:33], v[110:113], v[158:161], v[18:33]
	v_add_f32_e32 v10, 1.0, v3
	v_rcp_f32_e32 v3, v4
	v_add_f32_e32 v4, 1.0, v2
	v_rcp_f32_e32 v2, v8
	v_rcp_f32_e32 v183, v14
	v_rcp_f32_e32 v182, v16
	v_mfma_f32_32x32x16_bf16 v[18:33], v[106:109], v[154:157], v[18:33]
	v_add_f32_e32 v6, 1.0, v6
	v_add_f32_e32 v7, 1.0, v7
	v_rcp_f32_e32 v187, v10
	v_rcp_f32_e32 v186, v4
	v_exp_f32_e32 v190, v5
	v_exp_f32_e32 v191, v9
	v_mfma_f32_32x32x16_bf16 v[18:33], v[102:105], v[142:145], v[18:33]
	v_rcp_f32_e32 v189, v6
	v_rcp_f32_e32 v188, v7
	v_exp_f32_e32 v192, v13
	v_exp_f32_e32 v193, v17
	v_pk_fma_f32 v[4:5], v[178:179], s[12:13], v[184:185] op_sel_hi:[1,0,0]
	v_mfma_f32_32x32x16_bf16 v[18:33], v[98:101], v[130:133], v[18:33]
	v_mul_f32_e64 v178, v4, v2
	v_mul_f32_e64 v179, v5, v3
	v_pk_fma_f32 v[206:207], v[186:187], v[216:217], v[178:179]
	v_pk_fma_f32 v[178:179], v[180:181], s[12:13], v[184:185] op_sel_hi:[1,0,0]
	s_nop 0
	v_pk_mul_f32 v[178:179], v[178:179], v[182:183]
	s_nop 0
	v_pk_fma_f32 v[208:209], v[188:189], v[218:219], v[178:179]
	s_waitcnt lgkmcnt(4)
	v_mfma_f32_32x32x16_bf16 v[18:33], v[94:97], v[134:137], v[18:33]
	v_add_f32_e32 v178, 1.0, v190
	v_exp_f32_e32 v179, v207
	v_add_f32_e32 v180, 1.0, v191
	v_exp_f32_e32 v181, v206
	v_exp_f32_e32 v182, v209
	v_exp_f32_e32 v183, v208
	v_add_f32_e32 v184, 1.0, v192
	v_add_f32_e32 v185, 1.0, v193
	s_waitcnt lgkmcnt(3)
	v_mfma_f32_32x32x16_bf16 v[18:33], v[90:93], v[138:141], v[18:33]
	v_fmac_f32_e32 v178, v178, v179
	v_fmac_f32_e32 v180, v180, v181
	v_fmac_f32_e32 v184, v184, v182
	v_fmac_f32_e32 v185, v185, v183
	s_waitcnt lgkmcnt(2)
	v_mfma_f32_32x32x16_bf16 v[18:33], v[86:89], v[146:149], v[18:33]
	v_rcp_f32_e32 v178, v178
	v_rcp_f32_e32 v180, v180
	v_rcp_f32_e32 v184, v184
	v_rcp_f32_e32 v185, v185
	s_waitcnt lgkmcnt(1)
	v_mfma_f32_32x32x16_bf16 v[18:33], v[82:85], v[150:153], v[18:33]
	v_fma_f32 v178, -v179, v178, v178
	v_fma_f32 v179, -v181, v180, v180
	v_fma_f32 v180, -v182, v184, v184
	v_fma_f32 v181, -v183, v185, v185
	v_cvt_pk_bf16_f32 v178, v178, v179
	v_cvt_pk_bf16_f32 v179, v180, v181
	ds_write_b64 v211, v[178:179] offset:8200
	s_waitcnt lgkmcnt(0)
	s_barrier
	s_add_i32 s1, s1, 2
	s_cmp_gt_u32 s1, 16
	v_add_u32_e32 v232, 0x200, v232
	s_cbranch_scc1 .LBB1_30
.LBB1_14:
	s_waitcnt vmcnt(7)
	v_mfma_f32_32x32x16_bf16 v[2:17], v[78:81], v[174:177], v[236:251]
	v_add_u32_e32 v192, v230, v194
	ds_read_b32 v216, v232
	ds_read_b128 v[194:197], v210 offset:8192
	s_waitcnt vmcnt(6)
	v_mfma_f32_32x32x16_bf16 v[2:17], v[74:77], v[170:173], v[2:17]
	ds_read_b128 v[178:181], v210 offset:9216
	v_exp_f32_e32 v187, v20
	v_exp_f32_e32 v186, v24
	v_exp_f32_e32 v189, v28
	v_exp_f32_e32 v188, v32
	s_waitcnt vmcnt(5)
	v_mfma_f32_32x32x16_bf16 v[2:17], v[70:73], v[166:169], v[2:17]
	ds_read_b128 v[170:173], v210 offset:10240
	v_exp_f32_e32 v18, v18
	v_exp_f32_e32 v22, v22
	v_exp_f32_e32 v24, v26
	v_exp_f32_e32 v26, v30
	v_add_f32_e32 v20, 1.0, v187
	v_add_f32_e32 v28, 1.0, v186
	v_add_f32_e32 v30, 1.0, v189
	v_add_f32_e32 v32, 1.0, v188
	s_waitcnt vmcnt(4)
	v_mfma_f32_32x32x16_bf16 v[2:17], v[66:69], v[162:165], v[2:17]
	ds_read_b128 v[166:169], v210 offset:11264
	v_exp_f32_e32 v19, v19
	v_exp_f32_e32 v23, v23
	v_exp_f32_e32 v27, v27
	v_exp_f32_e32 v31, v31
	v_fmac_f32_e32 v20, v18, v20
	v_fmac_f32_e32 v28, v22, v28
	v_fmac_f32_e32 v30, v24, v30
	v_fmac_f32_e32 v32, v26, v32
	s_waitcnt vmcnt(3)
	v_mfma_f32_32x32x16_bf16 v[2:17], v[62:65], v[158:161], v[2:17]
	ds_read_b128 v[162:165], v210 offset:12288
	v_add_f32_e32 v22, 1.0, v19
	v_rcp_f32_e32 v19, v20
	v_rcp_f32_e32 v18, v28
	v_rcp_f32_e32 v191, v30
	v_rcp_f32_e32 v190, v32
	v_add_f32_e32 v20, 1.0, v23
	s_waitcnt vmcnt(2)
	v_mfma_f32_32x32x16_bf16 v[2:17], v[58:61], v[154:157], v[2:17]
	ds_read_b128 v[174:177], v210 offset:13312
	v_rcp_f32_e32 v159, v22
	v_rcp_f32_e32 v158, v20
	v_exp_f32_e32 v160, v21
	v_exp_f32_e32 v161, v25
	v_add_f32_e32 v23, 1.0, v27
	v_add_f32_e32 v20, 1.0, v31
	s_waitcnt vmcnt(1)
	v_mfma_f32_32x32x16_bf16 v[2:17], v[54:57], v[142:145], v[2:17]
	ds_read_b128 v[182:185], v210 offset:14336
	v_rcp_f32_e32 v155, v23
	v_rcp_f32_e32 v154, v20
	v_exp_f32_e32 v193, v29
	v_exp_f32_e32 v217, v33
	s_waitcnt vmcnt(0)
	v_mfma_f32_32x32x16_bf16 v[2:17], v[50:53], v[130:133], v[2:17]
	v_mov_b64_e32 v[218:219], s[0:1]
	v_fma_f32 v20, v186, s12, v218
	v_fma_f32 v21, v187, s12, v218
	ds_read_b128 v[142:145], v210 offset:15360
	v_mul_f32_e64 v156, v20, v18
	v_mul_f32_e64 v157, v21, v19
	ds_read_b128 v[18:21], v231 offset:36928
	ds_read_b128 v[22:25], v231 offset:36944
	ds_read_b128 v[26:29], v231 offset:36960
	ds_read_b128 v[30:33], v231 offset:36976
	v_pk_fma_f32 v[130:131], v[188:189], s[12:13], v[218:219] op_sel_hi:[1,0,0]
	v_pk_fma_f32 v[214:215], v[158:159], v[214:215], v[156:157]
	v_pk_mul_f32 v[130:131], v[130:131], v[190:191]
	s_nop 0
	v_pk_fma_f32 v[212:213], v[154:155], v[212:213], v[130:131]
	v_mfma_f32_32x32x16_bf16 v[2:17], v[46:49], v[134:137], v[2:17]
	ds_read_b128 v[154:157], v192 offset:16384
	v_add_f32_e32 v130, 1.0, v160
	v_exp_f32_e32 v131, v215
	v_exp_f32_e32 v132, v214
	v_exp_f32_e32 v133, v213
	v_exp_f32_e32 v220, v212
	v_add_f32_e32 v134, 1.0, v161
	v_add_f32_e32 v135, 1.0, v193
	v_add_f32_e32 v136, 1.0, v217
	v_mfma_f32_32x32x16_bf16 v[2:17], v[42:45], v[138:141], v[2:17]
	ds_read_b128 v[158:161], v192 offset:16416
	v_fmac_f32_e32 v130, v130, v131
	v_fmac_f32_e32 v134, v134, v132
	v_fmac_f32_e32 v135, v135, v133
	v_fmac_f32_e32 v136, v136, v220
	v_mfma_f32_32x32x16_bf16 v[2:17], v[38:41], v[146:149], v[2:17]
	ds_read_b128 v[186:189], v192 offset:16448
	v_rcp_f32_e32 v130, v130
	v_rcp_f32_e32 v134, v134
	v_rcp_f32_e32 v135, v135
	v_rcp_f32_e32 v136, v136
	v_mfma_f32_32x32x16_bf16 v[2:17], v[34:37], v[150:153], v[2:17]
	ds_read_b128 v[190:193], v192 offset:16480
	v_fma_f32 v130, -v131, v130, v130
	v_fma_f32 v131, -v132, v134, v134
	v_fma_f32 v132, -v133, v135, v135
	v_fma_f32 v133, -v220, v136, v136
	s_waitcnt lgkmcnt(4)
	v_mfma_f32_32x32x16_bf16 v[18:33], v[126:129], v[194:197], v[18:33]
	v_cvt_pk_bf16_f32 v130, v130, v131
	v_cvt_pk_bf16_f32 v131, v132, v133
	ds_write_b64 v211, v[130:131]
	v_mfma_f32_32x32x16_bf16 v[18:33], v[122:125], v[178:181], v[18:33]
	s_nop 1
	v_exp_f32_e32 v131, v4
	v_exp_f32_e32 v130, v8
	v_exp_f32_e32 v133, v12
	v_exp_f32_e32 v132, v16
	v_mfma_f32_32x32x16_bf16 v[18:33], v[118:121], v[170:173], v[18:33]
	v_exp_f32_e32 v2, v2
	v_exp_f32_e32 v6, v6
	v_exp_f32_e32 v10, v10
	v_exp_f32_e32 v12, v14
	v_add_f32_e32 v4, 1.0, v131
	v_add_f32_e32 v8, 1.0, v130
	v_add_f32_e32 v14, 1.0, v133
	v_add_f32_e32 v16, 1.0, v132
	v_mfma_f32_32x32x16_bf16 v[18:33], v[114:117], v[166:169], v[18:33]
	v_exp_f32_e32 v3, v3
	v_fmac_f32_e32 v4, v2, v4
	v_exp_f32_e32 v2, v7
	v_fmac_f32_e32 v8, v6, v8
	v_exp_f32_e32 v6, v11
	v_exp_f32_e32 v7, v15
	v_fmac_f32_e32 v14, v10, v14
	v_fmac_f32_e32 v16, v12, v16
	v_mfma_f32_32x32x16_bf16 v[18:33], v[110:113], v[162:165], v[18:33]
	v_add_f32_e32 v10, 1.0, v3
	v_rcp_f32_e32 v3, v4
	v_add_f32_e32 v4, 1.0, v2
	v_rcp_f32_e32 v2, v8
	v_rcp_f32_e32 v135, v14
	v_rcp_f32_e32 v134, v16
	v_mfma_f32_32x32x16_bf16 v[18:33], v[106:109], v[174:177], v[18:33]
	v_add_f32_e32 v6, 1.0, v6
	v_add_f32_e32 v7, 1.0, v7
	v_rcp_f32_e32 v137, v10
	v_rcp_f32_e32 v136, v4
	v_exp_f32_e32 v140, v5
	v_exp_f32_e32 v141, v9
	v_mfma_f32_32x32x16_bf16 v[18:33], v[102:105], v[182:185], v[18:33]
	v_rcp_f32_e32 v139, v6
	v_rcp_f32_e32 v138, v7
	v_exp_f32_e32 v146, v13
	v_exp_f32_e32 v147, v17
	v_pk_fma_f32 v[4:5], v[130:131], s[12:13], v[218:219] op_sel_hi:[1,0,0]
	v_mfma_f32_32x32x16_bf16 v[18:33], v[98:101], v[142:145], v[18:33]
	v_mul_f32_e64 v130, v4, v2
	v_mul_f32_e64 v131, v5, v3
	v_pk_fma_f32 v[224:225], v[136:137], v[204:205], v[130:131]
	v_pk_fma_f32 v[130:131], v[132:133], s[12:13], v[218:219] op_sel_hi:[1,0,0]
	s_nop 0
	v_pk_mul_f32 v[130:131], v[130:131], v[134:135]
	s_nop 0
	v_pk_fma_f32 v[226:227], v[138:139], v[202:203], v[130:131]
	s_waitcnt lgkmcnt(4)
	v_mfma_f32_32x32x16_bf16 v[18:33], v[94:97], v[154:157], v[18:33]
	v_add_f32_e32 v130, 1.0, v140
	v_exp_f32_e32 v131, v225
	v_add_f32_e32 v132, 1.0, v141
	v_exp_f32_e32 v133, v224
	v_exp_f32_e32 v134, v227
	v_exp_f32_e32 v135, v226
	v_add_f32_e32 v136, 1.0, v146
	v_add_f32_e32 v137, 1.0, v147
	s_waitcnt lgkmcnt(3)
	v_mfma_f32_32x32x16_bf16 v[18:33], v[90:93], v[158:161], v[18:33]
	v_fmac_f32_e32 v130, v130, v131
	v_fmac_f32_e32 v132, v132, v133
	v_fmac_f32_e32 v136, v136, v134
	v_fmac_f32_e32 v137, v137, v135
	s_waitcnt lgkmcnt(2)
	v_mfma_f32_32x32x16_bf16 v[18:33], v[86:89], v[186:189], v[18:33]
	v_rcp_f32_e32 v130, v130
	v_rcp_f32_e32 v132, v132
	v_rcp_f32_e32 v136, v136
	v_rcp_f32_e32 v137, v137
	s_waitcnt lgkmcnt(1)
	v_mfma_f32_32x32x16_bf16 v[18:33], v[82:85], v[190:193], v[18:33]
	v_fma_f32 v130, -v131, v130, v130
	v_fma_f32 v131, -v133, v132, v132
	v_fma_f32 v132, -v134, v136, v136
	v_fma_f32 v133, -v135, v137, v137
	v_cvt_pk_bf16_f32 v130, v130, v131
	v_cvt_pk_bf16_f32 v131, v132, v133
	ds_write_b64 v211, v[130:131] offset:8
	s_waitcnt lgkmcnt(0)
	s_barrier
	v_mfma_f32_32x32x16_bf16 v[2:17], v[78:81], v[194:197], v[236:251]
	ds_read_b32 v233, v232 offset:128
	ds_read_b128 v[202:205], v210
	v_add_u32_e32 v216, v230, v216
	v_mfma_f32_32x32x16_bf16 v[2:17], v[74:77], v[178:181], v[2:17]
	ds_read_b128 v[194:197], v210 offset:1024
	v_exp_f32_e32 v147, v20
	v_exp_f32_e32 v146, v24
	v_exp_f32_e32 v149, v28
	v_exp_f32_e32 v148, v32
	v_mfma_f32_32x32x16_bf16 v[2:17], v[70:73], v[170:173], v[2:17]
	ds_read_b128 v[138:141], v210 offset:2048
	v_exp_f32_e32 v18, v18
	v_exp_f32_e32 v22, v22
	v_exp_f32_e32 v24, v26
	v_exp_f32_e32 v26, v30
	v_add_f32_e32 v20, 1.0, v147
	v_add_f32_e32 v28, 1.0, v146
	v_add_f32_e32 v30, 1.0, v149
	v_add_f32_e32 v32, 1.0, v148
	v_mfma_f32_32x32x16_bf16 v[2:17], v[66:69], v[166:169], v[2:17]
	ds_read_b128 v[134:137], v210 offset:3072
	v_exp_f32_e32 v19, v19
	v_exp_f32_e32 v23, v23
	v_exp_f32_e32 v27, v27
	v_exp_f32_e32 v31, v31
	v_fmac_f32_e32 v20, v18, v20
	v_fmac_f32_e32 v28, v22, v28
	v_fmac_f32_e32 v30, v24, v30
	v_fmac_f32_e32 v32, v26, v32
	v_mfma_f32_32x32x16_bf16 v[2:17], v[62:65], v[162:165], v[2:17]
	ds_read_b128 v[166:169], v210 offset:4096
	v_add_f32_e32 v22, 1.0, v19
	v_rcp_f32_e32 v19, v20
	v_rcp_f32_e32 v18, v28
	v_rcp_f32_e32 v151, v30
	v_rcp_f32_e32 v150, v32
	v_add_f32_e32 v20, 1.0, v23
	v_mfma_f32_32x32x16_bf16 v[2:17], v[58:61], v[174:177], v[2:17]
	ds_read_b128 v[162:165], v210 offset:5120
	v_rcp_f32_e32 v153, v22
	v_rcp_f32_e32 v152, v20
	v_add_f32_e32 v23, 1.0, v27
	v_add_f32_e32 v20, 1.0, v31
	v_exp_f32_e32 v180, v21
	v_exp_f32_e32 v181, v25
	v_mfma_f32_32x32x16_bf16 v[2:17], v[54:57], v[182:185], v[2:17]
	ds_read_b128 v[170:173], v210 offset:6144
	v_rcp_f32_e32 v175, v23
	v_rcp_f32_e32 v174, v20
	v_exp_f32_e32 v176, v29
	v_exp_f32_e32 v177, v33
	v_mfma_f32_32x32x16_bf16 v[2:17], v[50:53], v[142:145], v[2:17]
	v_mov_b64_e32 v[178:179], s[0:1]
	v_fma_f32 v20, v146, s12, v178
	v_fma_f32 v21, v147, s12, v178
	ds_read_b128 v[130:133], v210 offset:7168
	v_mul_f32_e64 v146, v20, v18
	v_mul_f32_e64 v147, v21, v19
	ds_read_b128 v[18:21], v231 offset:36928
	ds_read_b128 v[22:25], v231 offset:36944
	ds_read_b128 v[26:29], v231 offset:36960
	ds_read_b128 v[30:33], v231 offset:36976
	v_pk_fma_f32 v[142:143], v[148:149], s[12:13], v[178:179] op_sel_hi:[1,0,0]
	v_pk_fma_f32 v[220:221], v[152:153], v[200:201], v[146:147]
	v_pk_mul_f32 v[142:143], v[142:143], v[150:151]
	s_nop 0
	v_pk_fma_f32 v[222:223], v[174:175], v[198:199], v[142:143]
	v_mfma_f32_32x32x16_bf16 v[2:17], v[46:49], v[154:157], v[2:17]
	ds_read_b128 v[146:149], v216 offset:16384
	v_add_f32_e32 v142, 1.0, v180
	v_exp_f32_e32 v143, v221
	v_exp_f32_e32 v144, v220
	v_exp_f32_e32 v145, v223
	v_exp_f32_e32 v180, v222
	v_add_f32_e32 v154, 1.0, v181
	v_add_f32_e32 v155, 1.0, v176
	v_add_f32_e32 v156, 1.0, v177
	v_mfma_f32_32x32x16_bf16 v[2:17], v[42:45], v[158:161], v[2:17]
	ds_read_b128 v[150:153], v216 offset:16416
	v_fmac_f32_e32 v142, v142, v143
	v_fmac_f32_e32 v154, v154, v144
	v_fmac_f32_e32 v155, v155, v145
	v_fmac_f32_e32 v156, v156, v180
	v_mfma_f32_32x32x16_bf16 v[2:17], v[38:41], v[186:189], v[2:17]
	ds_read_b128 v[174:177], v216 offset:16448
	v_rcp_f32_e32 v142, v142
	v_rcp_f32_e32 v154, v154
	v_rcp_f32_e32 v155, v155
	v_rcp_f32_e32 v156, v156
	v_mfma_f32_32x32x16_bf16 v[2:17], v[34:37], v[190:193], v[2:17]
	ds_read_b128 v[198:201], v216 offset:16480
	v_fma_f32 v142, -v143, v142, v142
	v_fma_f32 v143, -v144, v154, v154
	v_fma_f32 v144, -v145, v155, v155
	v_fma_f32 v145, -v180, v156, v156
	s_waitcnt lgkmcnt(4)
	v_mfma_f32_32x32x16_bf16 v[18:33], v[126:129], v[202:205], v[18:33]
	v_cvt_pk_bf16_f32 v142, v142, v143
	v_cvt_pk_bf16_f32 v143, v144, v145
	ds_write_b64 v211, v[142:143] offset:8192
	v_mfma_f32_32x32x16_bf16 v[18:33], v[122:125], v[194:197], v[18:33]
	s_nop 1
	v_exp_f32_e32 v143, v4
	v_exp_f32_e32 v142, v8
	v_exp_f32_e32 v145, v12
	v_exp_f32_e32 v144, v16
	v_mfma_f32_32x32x16_bf16 v[18:33], v[118:121], v[138:141], v[18:33]
	v_exp_f32_e32 v2, v2
	v_exp_f32_e32 v6, v6
	v_exp_f32_e32 v10, v10
	v_exp_f32_e32 v12, v14
	v_add_f32_e32 v4, 1.0, v143
	v_add_f32_e32 v8, 1.0, v142
	v_add_f32_e32 v14, 1.0, v145
	v_add_f32_e32 v16, 1.0, v144
	v_mfma_f32_32x32x16_bf16 v[18:33], v[114:117], v[134:137], v[18:33]
	v_exp_f32_e32 v3, v3
	v_fmac_f32_e32 v4, v2, v4
	v_exp_f32_e32 v2, v7
	v_fmac_f32_e32 v8, v6, v8
	v_exp_f32_e32 v6, v11
	v_exp_f32_e32 v7, v15
	v_fmac_f32_e32 v14, v10, v14
	v_fmac_f32_e32 v16, v12, v16
	v_mfma_f32_32x32x16_bf16 v[18:33], v[110:113], v[166:169], v[18:33]
	v_add_f32_e32 v10, 1.0, v3
	v_rcp_f32_e32 v3, v4
	v_add_f32_e32 v4, 1.0, v2
	v_rcp_f32_e32 v2, v8
	v_rcp_f32_e32 v155, v14
	v_rcp_f32_e32 v154, v16
	v_mfma_f32_32x32x16_bf16 v[18:33], v[106:109], v[162:165], v[18:33]
	v_add_f32_e32 v6, 1.0, v6
	v_add_f32_e32 v7, 1.0, v7
	v_rcp_f32_e32 v157, v10
	v_rcp_f32_e32 v156, v4
	v_exp_f32_e32 v160, v5
	v_exp_f32_e32 v161, v9
	v_mfma_f32_32x32x16_bf16 v[18:33], v[102:105], v[170:173], v[18:33]
	v_rcp_f32_e32 v159, v6
	v_rcp_f32_e32 v158, v7
	v_exp_f32_e32 v180, v13
	v_exp_f32_e32 v181, v17
	v_pk_fma_f32 v[4:5], v[142:143], s[12:13], v[178:179] op_sel_hi:[1,0,0]
	v_mfma_f32_32x32x16_bf16 v[18:33], v[98:101], v[130:133], v[18:33]
	v_mul_f32_e64 v142, v4, v2
	v_mul_f32_e64 v143, v5, v3
	v_pk_fma_f32 v[216:217], v[156:157], v[206:207], v[142:143]
	v_pk_fma_f32 v[142:143], v[144:145], s[12:13], v[178:179] op_sel_hi:[1,0,0]
	s_nop 0
	v_pk_mul_f32 v[142:143], v[142:143], v[154:155]
	s_nop 0
	v_pk_fma_f32 v[218:219], v[158:159], v[208:209], v[142:143]
	s_waitcnt lgkmcnt(4)
	v_mfma_f32_32x32x16_bf16 v[18:33], v[94:97], v[146:149], v[18:33]
	v_add_f32_e32 v142, 1.0, v160
	v_exp_f32_e32 v143, v217
	v_add_f32_e32 v144, 1.0, v161
	v_exp_f32_e32 v145, v216
	v_exp_f32_e32 v154, v219
	v_exp_f32_e32 v155, v218
	v_add_f32_e32 v156, 1.0, v180
	v_add_f32_e32 v157, 1.0, v181
	s_waitcnt lgkmcnt(3)
	v_mfma_f32_32x32x16_bf16 v[18:33], v[90:93], v[150:153], v[18:33]
	v_fmac_f32_e32 v142, v142, v143
	v_fmac_f32_e32 v144, v144, v145
	v_fmac_f32_e32 v156, v156, v154
	v_fmac_f32_e32 v157, v157, v155
	s_waitcnt lgkmcnt(2)
	v_mfma_f32_32x32x16_bf16 v[18:33], v[86:89], v[174:177], v[18:33]
	v_rcp_f32_e32 v142, v142
	v_rcp_f32_e32 v144, v144
	v_rcp_f32_e32 v156, v156
	v_rcp_f32_e32 v157, v157
	s_waitcnt lgkmcnt(1)
	v_mfma_f32_32x32x16_bf16 v[18:33], v[82:85], v[198:201], v[18:33]
	v_fma_f32 v142, -v143, v142, v142
	v_fma_f32 v143, -v145, v144, v144
	v_fma_f32 v144, -v154, v156, v156
	v_fma_f32 v145, -v155, v157, v157
	v_cvt_pk_bf16_f32 v142, v142, v143
	v_cvt_pk_bf16_f32 v143, v144, v145
	ds_write_b64 v211, v[142:143] offset:8200
	s_waitcnt lgkmcnt(0)
	s_barrier
	v_mfma_f32_32x32x16_bf16 v[2:17], v[78:81], v[202:205], v[236:251]
	v_add_u32_e32 v234, v230, v233
	ds_read_b32 v233, v232 offset:256
	ds_read_b128 v[206:209], v210 offset:8192
	v_mfma_f32_32x32x16_bf16 v[2:17], v[74:77], v[194:197], v[2:17]
	ds_read_b128 v[190:193], v210 offset:9216
	v_exp_f32_e32 v179, v20
	v_exp_f32_e32 v178, v24
	v_exp_f32_e32 v181, v28
	v_exp_f32_e32 v180, v32
	v_mfma_f32_32x32x16_bf16 v[2:17], v[70:73], v[138:141], v[2:17]
	ds_read_b128 v[158:161], v210 offset:10240
	v_exp_f32_e32 v18, v18
	v_exp_f32_e32 v22, v22
	v_exp_f32_e32 v24, v26
	v_exp_f32_e32 v26, v30
	v_add_f32_e32 v20, 1.0, v179
	v_add_f32_e32 v28, 1.0, v178
	v_add_f32_e32 v30, 1.0, v181
	v_add_f32_e32 v32, 1.0, v180
	v_mfma_f32_32x32x16_bf16 v[2:17], v[66:69], v[134:137], v[2:17]
	ds_read_b128 v[142:145], v210 offset:11264
	v_exp_f32_e32 v19, v19
	v_exp_f32_e32 v23, v23
	v_exp_f32_e32 v27, v27
	v_exp_f32_e32 v31, v31
	v_fmac_f32_e32 v20, v18, v20
	v_fmac_f32_e32 v28, v22, v28
	v_fmac_f32_e32 v30, v24, v30
	v_fmac_f32_e32 v32, v26, v32
	v_mfma_f32_32x32x16_bf16 v[2:17], v[62:65], v[166:169], v[2:17]
	ds_read_b128 v[154:157], v210 offset:12288
	v_add_f32_e32 v22, 1.0, v19
	v_rcp_f32_e32 v19, v20
	v_rcp_f32_e32 v18, v28
	v_rcp_f32_e32 v139, v30
	v_rcp_f32_e32 v138, v32
	v_add_f32_e32 v20, 1.0, v23
	v_mfma_f32_32x32x16_bf16 v[2:17], v[58:61], v[162:165], v[2:17]
	ds_read_b128 v[182:185], v210 offset:13312
	v_rcp_f32_e32 v141, v22
	v_rcp_f32_e32 v140, v20
	v_add_f32_e32 v23, 1.0, v27
	v_add_f32_e32 v20, 1.0, v31
	v_exp_f32_e32 v168, v21
	v_exp_f32_e32 v169, v25
	v_mfma_f32_32x32x16_bf16 v[2:17], v[54:57], v[170:173], v[2:17]
	ds_read_b128 v[186:189], v210 offset:14336
	v_rcp_f32_e32 v163, v23
	v_rcp_f32_e32 v162, v20
	v_exp_f32_e32 v194, v29
	v_exp_f32_e32 v195, v33
	v_mfma_f32_32x32x16_bf16 v[2:17], v[50:53], v[130:133], v[2:17]
	v_mov_b64_e32 v[164:165], s[0:1]
	v_fma_f32 v20, v178, s12, v164
	v_fma_f32 v21, v179, s12, v164
	ds_read_b128 v[134:137], v210 offset:15360
	v_mul_f32_e64 v166, v20, v18
	v_mul_f32_e64 v167, v21, v19
	ds_read_b128 v[18:21], v231 offset:36928
	ds_read_b128 v[22:25], v231 offset:36944
	ds_read_b128 v[26:29], v231 offset:36960
	ds_read_b128 v[30:33], v231 offset:36976
	v_pk_fma_f32 v[130:131], v[180:181], s[12:13], v[164:165] op_sel_hi:[1,0,0]
	v_pk_fma_f32 v[214:215], v[140:141], v[214:215], v[166:167]
	v_pk_mul_f32 v[130:131], v[130:131], v[138:139]
	s_nop 0
	v_pk_fma_f32 v[212:213], v[162:163], v[212:213], v[130:131]
	v_mfma_f32_32x32x16_bf16 v[2:17], v[46:49], v[146:149], v[2:17]
	ds_read_b128 v[138:141], v234 offset:16384
	v_add_f32_e32 v130, 1.0, v168
	v_exp_f32_e32 v131, v215
	v_exp_f32_e32 v132, v214
	v_exp_f32_e32 v133, v213
	v_exp_f32_e32 v162, v212
	v_add_f32_e32 v163, 1.0, v169
	v_add_f32_e32 v166, 1.0, v194
	v_add_f32_e32 v167, 1.0, v195
	v_mfma_f32_32x32x16_bf16 v[2:17], v[42:45], v[150:153], v[2:17]
	ds_read_b128 v[146:149], v234 offset:16416
	v_fmac_f32_e32 v130, v130, v131
	v_fmac_f32_e32 v163, v163, v132
	v_fmac_f32_e32 v166, v166, v133
	v_fmac_f32_e32 v167, v167, v162
	v_mfma_f32_32x32x16_bf16 v[2:17], v[38:41], v[174:177], v[2:17]
	ds_read_b128 v[150:153], v234 offset:16448
	v_rcp_f32_e32 v130, v130
	v_rcp_f32_e32 v163, v163
	v_rcp_f32_e32 v166, v166
	v_rcp_f32_e32 v167, v167
	v_mfma_f32_32x32x16_bf16 v[2:17], v[34:37], v[198:201], v[2:17]
	ds_read_b128 v[178:181], v234 offset:16480
	v_fma_f32 v130, -v131, v130, v130
	v_fma_f32 v131, -v132, v163, v163
	v_fma_f32 v132, -v133, v166, v166
	v_fma_f32 v133, -v162, v167, v167
	s_waitcnt lgkmcnt(4)
	v_mfma_f32_32x32x16_bf16 v[18:33], v[126:129], v[206:209], v[18:33]
	v_cvt_pk_bf16_f32 v130, v130, v131
	v_cvt_pk_bf16_f32 v131, v132, v133
	ds_write_b64 v211, v[130:131]
	v_mfma_f32_32x32x16_bf16 v[18:33], v[122:125], v[190:193], v[18:33]
	s_nop 1
	v_exp_f32_e32 v131, v4
	v_exp_f32_e32 v130, v8
	v_exp_f32_e32 v133, v12
	v_exp_f32_e32 v132, v16
	v_mfma_f32_32x32x16_bf16 v[18:33], v[118:121], v[158:161], v[18:33]
	v_exp_f32_e32 v2, v2
	v_exp_f32_e32 v6, v6
	v_exp_f32_e32 v10, v10
	v_exp_f32_e32 v12, v14
	v_add_f32_e32 v4, 1.0, v131
	v_add_f32_e32 v8, 1.0, v130
	v_add_f32_e32 v14, 1.0, v133
	v_add_f32_e32 v16, 1.0, v132
	v_mfma_f32_32x32x16_bf16 v[18:33], v[114:117], v[142:145], v[18:33]
	v_exp_f32_e32 v3, v3
	v_fmac_f32_e32 v4, v2, v4
	v_exp_f32_e32 v2, v7
	v_fmac_f32_e32 v8, v6, v8
	v_exp_f32_e32 v6, v11
	v_exp_f32_e32 v7, v15
	v_fmac_f32_e32 v14, v10, v14
	v_fmac_f32_e32 v16, v12, v16
	v_mfma_f32_32x32x16_bf16 v[18:33], v[110:113], v[154:157], v[18:33]
	v_add_f32_e32 v10, 1.0, v3
	v_rcp_f32_e32 v3, v4
	v_add_f32_e32 v4, 1.0, v2
	v_rcp_f32_e32 v2, v8
	v_rcp_f32_e32 v163, v14
	v_rcp_f32_e32 v162, v16
	v_mfma_f32_32x32x16_bf16 v[18:33], v[106:109], v[182:185], v[18:33]
	v_add_f32_e32 v6, 1.0, v6
	v_add_f32_e32 v7, 1.0, v7
	v_rcp_f32_e32 v167, v10
	v_rcp_f32_e32 v166, v4
	v_exp_f32_e32 v170, v5
	v_exp_f32_e32 v171, v9
	v_mfma_f32_32x32x16_bf16 v[18:33], v[102:105], v[186:189], v[18:33]
	v_rcp_f32_e32 v169, v6
	v_rcp_f32_e32 v168, v7
	v_exp_f32_e32 v172, v13
	v_exp_f32_e32 v173, v17
	v_pk_fma_f32 v[4:5], v[130:131], s[12:13], v[164:165] op_sel_hi:[1,0,0]
	v_mfma_f32_32x32x16_bf16 v[18:33], v[98:101], v[134:137], v[18:33]
	v_mul_f32_e64 v130, v4, v2
	v_mul_f32_e64 v131, v5, v3
	v_pk_fma_f32 v[204:205], v[166:167], v[224:225], v[130:131]
	v_pk_fma_f32 v[130:131], v[132:133], s[12:13], v[164:165] op_sel_hi:[1,0,0]
	s_nop 0
	v_pk_mul_f32 v[130:131], v[130:131], v[162:163]
	s_nop 0
	v_pk_fma_f32 v[202:203], v[168:169], v[226:227], v[130:131]
	s_waitcnt lgkmcnt(4)
	v_mfma_f32_32x32x16_bf16 v[18:33], v[94:97], v[138:141], v[18:33]
	v_add_f32_e32 v130, 1.0, v170
	v_exp_f32_e32 v131, v205
	v_add_f32_e32 v132, 1.0, v171
	v_exp_f32_e32 v133, v204
	v_exp_f32_e32 v162, v203
	v_exp_f32_e32 v163, v202
	v_add_f32_e32 v164, 1.0, v172
	v_add_f32_e32 v165, 1.0, v173
	s_waitcnt lgkmcnt(3)
	v_mfma_f32_32x32x16_bf16 v[18:33], v[90:93], v[146:149], v[18:33]
	v_fmac_f32_e32 v130, v130, v131
	v_fmac_f32_e32 v132, v132, v133
	v_fmac_f32_e32 v164, v164, v162
	v_fmac_f32_e32 v165, v165, v163
	s_waitcnt lgkmcnt(2)
	v_mfma_f32_32x32x16_bf16 v[18:33], v[86:89], v[150:153], v[18:33]
	v_rcp_f32_e32 v130, v130
	v_rcp_f32_e32 v132, v132
	v_rcp_f32_e32 v164, v164
	v_rcp_f32_e32 v165, v165
	s_waitcnt lgkmcnt(1)
	v_mfma_f32_32x32x16_bf16 v[18:33], v[82:85], v[178:181], v[18:33]
	v_fma_f32 v130, -v131, v130, v130
	v_fma_f32 v131, -v133, v132, v132
	v_fma_f32 v132, -v162, v164, v164
	v_fma_f32 v133, -v163, v165, v165
	v_cvt_pk_bf16_f32 v130, v130, v131
	v_cvt_pk_bf16_f32 v131, v132, v133
	ds_write_b64 v211, v[130:131] offset:8
	s_waitcnt lgkmcnt(0)
	s_barrier
	s_branch .LBB1_13
.LBB1_30:
	v_mfma_f32_32x32x16_bf16 v[2:17], v[78:81], v[174:177], v[236:251]
	ds_read_b128 v[178:181], v210 offset:8192
	v_add_u32_e32 v182, v230, v194
	v_mfma_f32_32x32x16_bf16 v[2:17], v[74:77], v[170:173], v[2:17]
	ds_read_b128 v[174:177], v210 offset:9216
	v_exp_f32_e32 v20, v20
	v_exp_f32_e32 v24, v24
	v_exp_f32_e32 v28, v28
	v_exp_f32_e32 v32, v32
	v_mfma_f32_32x32x16_bf16 v[2:17], v[70:73], v[166:169], v[2:17]
	ds_read_b128 v[170:173], v210 offset:10240
	v_exp_f32_e32 v18, v18
	v_exp_f32_e32 v22, v22
	v_exp_f32_e32 v26, v26
	v_exp_f32_e32 v30, v30
	v_add_f32_e32 v183, 1.0, v20
	v_add_f32_e32 v184, 1.0, v24
	v_add_f32_e32 v185, 1.0, v28
	v_add_f32_e32 v186, 1.0, v32
	v_mfma_f32_32x32x16_bf16 v[2:17], v[66:69], v[162:165], v[2:17]
	ds_read_b128 v[166:169], v210 offset:11264
	v_exp_f32_e32 v19, v19
	v_fmac_f32_e32 v183, v18, v183
	v_exp_f32_e32 v18, v23
	v_exp_f32_e32 v23, v27
	v_exp_f32_e32 v27, v31
	v_fmac_f32_e32 v184, v22, v184
	v_fmac_f32_e32 v185, v26, v185
	v_fmac_f32_e32 v186, v30, v186
	v_mfma_f32_32x32x16_bf16 v[2:17], v[62:65], v[158:161], v[2:17]
	ds_read_b128 v[162:165], v210 offset:12288
	v_rcp_f32_e32 v22, v183
	v_rcp_f32_e32 v26, v184
	v_rcp_f32_e32 v30, v185
	v_rcp_f32_e32 v31, v186
	v_mov_b32_e32 v183, 0xc038aa3b
	v_add_f32_e32 v19, 1.0, v19
	v_fmamk_f32 v20, v20, 0x4038aa3b, v183
	v_add_f32_e32 v18, 1.0, v18
	v_fmamk_f32 v24, v24, 0x4038aa3b, v183
	v_mfma_f32_32x32x16_bf16 v[2:17], v[58:61], v[154:157], v[2:17]
	ds_read_b128 v[158:161], v210 offset:13312
	v_rcp_f32_e32 v19, v19
	v_add_f32_e32 v23, 1.0, v23
	v_rcp_f32_e32 v184, v18
	v_exp_f32_e32 v185, v21
	v_exp_f32_e32 v186, v25
	v_fmamk_f32 v18, v28, 0x4038aa3b, v183
	v_add_f32_e32 v21, 1.0, v27
	v_fmamk_f32 v25, v32, 0x4038aa3b, v183
	v_mfma_f32_32x32x16_bf16 v[2:17], v[54:57], v[142:145], v[2:17]
	ds_read_b128 v[154:157], v210 offset:14336
	v_mul_f32_e32 v187, v20, v22
	v_rcp_f32_e32 v188, v23
	v_rcp_f32_e32 v189, v21
	v_exp_f32_e32 v190, v29
	v_exp_f32_e32 v191, v33
	v_mul_f32_e32 v192, v24, v26
	v_mul_f32_e32 v193, v18, v30
	v_mul_f32_e32 v194, v25, v31
	v_mfma_f32_32x32x16_bf16 v[2:17], v[50:53], v[130:133], v[2:17]
	ds_read_b128 v[142:145], v210 offset:15360
	v_fmac_f32_e32 v187, v19, v215
	ds_read_b128 v[18:21], v231 offset:36928
	ds_read_b128 v[22:25], v231 offset:36944
	ds_read_b128 v[26:29], v231 offset:36960
	ds_read_b128 v[30:33], v231 offset:36976
	v_fmac_f32_e32 v192, v184, v214
	v_fmac_f32_e32 v193, v188, v213
	v_fmac_f32_e32 v194, v189, v212
	v_mfma_f32_32x32x16_bf16 v[2:17], v[46:49], v[134:137], v[2:17]
	ds_read_b128 v[130:133], v182 offset:16384
	v_add_f32_e32 v184, 1.0, v185
	v_exp_f32_e32 v185, v187
	v_exp_f32_e32 v187, v192
	v_exp_f32_e32 v188, v193
	v_exp_f32_e32 v189, v194
	v_add_f32_e32 v186, 1.0, v186
	v_add_f32_e32 v190, 1.0, v190
	v_add_f32_e32 v191, 1.0, v191
	v_mfma_f32_32x32x16_bf16 v[2:17], v[42:45], v[138:141], v[2:17]
	ds_read_b128 v[134:137], v182 offset:16416
	v_fmac_f32_e32 v184, v184, v185
	v_fmac_f32_e32 v186, v186, v187
	v_fmac_f32_e32 v190, v190, v188
	v_fmac_f32_e32 v191, v191, v189
	v_mfma_f32_32x32x16_bf16 v[2:17], v[38:41], v[146:149], v[2:17]
	ds_read_b128 v[138:141], v182 offset:16448
	v_rcp_f32_e32 v184, v184
	v_rcp_f32_e32 v186, v186
	v_rcp_f32_e32 v190, v190
	v_rcp_f32_e32 v191, v191
	v_mfma_f32_32x32x16_bf16 v[2:17], v[34:37], v[150:153], v[2:17]
	ds_read_b128 v[146:149], v182 offset:16480
	v_fma_f32 v182, -v185, v184, v184
	v_fma_f32 v184, -v187, v186, v186
	v_fma_f32 v185, -v188, v190, v190
	v_fma_f32 v186, -v189, v191, v191
	s_waitcnt lgkmcnt(4)
	v_mfma_f32_32x32x16_bf16 v[18:33], v[126:129], v[178:181], v[18:33]
	v_cvt_pk_bf16_f32 v150, v182, v184
	v_cvt_pk_bf16_f32 v151, v185, v186
	ds_write_b64 v211, v[150:151]
	v_mfma_f32_32x32x16_bf16 v[18:33], v[122:125], v[174:177], v[18:33]
	s_nop 1
	v_exp_f32_e32 v4, v4
	v_exp_f32_e32 v8, v8
	v_exp_f32_e32 v12, v12
	v_exp_f32_e32 v16, v16
	v_mfma_f32_32x32x16_bf16 v[18:33], v[118:121], v[170:173], v[18:33]
	v_exp_f32_e32 v2, v2
	v_exp_f32_e32 v6, v6
	v_exp_f32_e32 v10, v10
	v_exp_f32_e32 v14, v14
	v_add_f32_e32 v122, 1.0, v4
	v_add_f32_e32 v123, 1.0, v8
	v_add_f32_e32 v118, 1.0, v12
	v_add_f32_e32 v119, 1.0, v16
	v_mfma_f32_32x32x16_bf16 v[18:33], v[114:117], v[166:169], v[18:33]
	v_exp_f32_e32 v3, v3
	v_fmac_f32_e32 v122, v2, v122
	v_exp_f32_e32 v2, v7
	v_fmac_f32_e32 v123, v6, v123
	v_exp_f32_e32 v6, v11
	v_exp_f32_e32 v7, v15
	v_fmac_f32_e32 v118, v10, v118
	v_fmac_f32_e32 v119, v14, v119
	v_mfma_f32_32x32x16_bf16 v[18:33], v[110:113], v[162:165], v[18:33]
	v_rcp_f32_e32 v10, v122
	v_rcp_f32_e32 v11, v123
	v_rcp_f32_e32 v14, v118
	v_rcp_f32_e32 v15, v119
	v_add_f32_e32 v3, 1.0, v3
	v_fmamk_f32 v4, v4, 0x4038aa3b, v183
	v_add_f32_e32 v2, 1.0, v2
	v_fmamk_f32 v8, v8, 0x4038aa3b, v183
	v_mfma_f32_32x32x16_bf16 v[18:33], v[106:109], v[158:161], v[18:33]
	v_rcp_f32_e32 v3, v3
	v_rcp_f32_e32 v2, v2
	v_add_f32_e32 v6, 1.0, v6
	v_fmamk_f32 v12, v12, 0x4038aa3b, v183
	v_exp_f32_e32 v110, v5
	v_add_f32_e32 v5, 1.0, v7
	v_exp_f32_e32 v111, v9
	v_fmac_f32_e32 v183, 0x4038aa3b, v16
	v_mfma_f32_32x32x16_bf16 v[18:33], v[102:105], v[154:157], v[18:33]
	v_mul_f32_e32 v106, v4, v10
	v_mul_f32_e32 v107, v8, v11
	v_rcp_f32_e32 v108, v6
	v_rcp_f32_e32 v109, v5
	v_exp_f32_e32 v112, v13
	v_exp_f32_e32 v113, v17
	v_mul_f32_e32 v102, v12, v14
	v_mul_f32_e32 v103, v183, v15
	v_mfma_f32_32x32x16_bf16 v[18:33], v[98:101], v[142:145], v[18:33]
	v_fmac_f32_e32 v106, v3, v205
	v_fmac_f32_e32 v107, v2, v204
	v_fmac_f32_e32 v102, v108, v203
	v_fmac_f32_e32 v103, v109, v202
	s_waitcnt lgkmcnt(4)
	v_mfma_f32_32x32x16_bf16 v[18:33], v[94:97], v[130:133], v[18:33]
	v_add_f32_e32 v98, 1.0, v110
	v_exp_f32_e32 v99, v106
	v_add_f32_e32 v100, 1.0, v111
	v_exp_f32_e32 v101, v107
	v_exp_f32_e32 v102, v102
	v_exp_f32_e32 v103, v103
	v_add_f32_e32 v94, 1.0, v112
	v_add_f32_e32 v95, 1.0, v113
	s_waitcnt lgkmcnt(3)
	v_mfma_f32_32x32x16_bf16 v[18:33], v[90:93], v[134:137], v[18:33]
	v_fmac_f32_e32 v98, v98, v99
	v_fmac_f32_e32 v100, v100, v101
	v_fmac_f32_e32 v94, v94, v102
	v_fmac_f32_e32 v95, v95, v103
	s_waitcnt lgkmcnt(2)
	v_mfma_f32_32x32x16_bf16 v[18:33], v[86:89], v[138:141], v[18:33]
	v_rcp_f32_e32 v90, v98
	v_rcp_f32_e32 v91, v100
	v_rcp_f32_e32 v92, v94
	v_rcp_f32_e32 v93, v95
	s_waitcnt lgkmcnt(1)
	v_mfma_f32_32x32x16_bf16 v[18:33], v[82:85], v[146:149], v[18:33]
	v_fma_f32 v86, -v99, v90, v90
	v_fma_f32 v87, -v101, v91, v91
	v_fma_f32 v88, -v102, v92, v92
	v_fma_f32 v89, -v103, v93, v93
	v_cvt_pk_bf16_f32 v82, v86, v87
	v_cvt_pk_bf16_f32 v83, v88, v89
	ds_write_b64 v211, v[82:83] offset:8
	s_waitcnt lgkmcnt(0)
	s_barrier
	v_mfma_f32_32x32x16_bf16 v[2:17], v[78:81], v[178:181], v[236:251]
	v_exp_f32_e32 v20, v20
	v_exp_f32_e32 v24, v24
	v_exp_f32_e32 v28, v28
	v_exp_f32_e32 v32, v32
	v_mfma_f32_32x32x16_bf16 v[2:17], v[74:77], v[174:177], v[2:17]
	v_exp_f32_e32 v18, v18
	v_add_f32_e32 v74, 1.0, v20
	v_exp_f32_e32 v22, v22
	v_add_f32_e32 v75, 1.0, v24
	v_exp_f32_e32 v26, v26
	v_exp_f32_e32 v30, v30
	v_mfma_f32_32x32x16_bf16 v[2:17], v[70:73], v[170:173], v[2:17]
	v_add_f32_e32 v70, 1.0, v28
	v_add_f32_e32 v71, 1.0, v32
	v_exp_f32_e32 v19, v19
	v_fmac_f32_e32 v74, v18, v74
	v_exp_f32_e32 v18, v23
	v_fmac_f32_e32 v75, v22, v75
	v_exp_f32_e32 v22, v27
	v_exp_f32_e32 v23, v31
	v_mfma_f32_32x32x16_bf16 v[2:17], v[66:69], v[166:169], v[2:17]
	v_fmac_f32_e32 v70, v26, v70
	v_fmac_f32_e32 v71, v30, v71
	v_mov_b32_e32 v27, 0xc038aa3b
	v_add_f32_e32 v19, 1.0, v19
	v_rcp_f32_e32 v26, v74
	v_rcp_f32_e32 v30, v75
	v_rcp_f32_e32 v31, v70
	v_rcp_f32_e32 v66, v71
	v_mfma_f32_32x32x16_bf16 v[2:17], v[62:65], v[162:165], v[2:17]
	v_fmamk_f32 v20, v20, 0x4038aa3b, v27
	v_add_f32_e32 v18, 1.0, v18
	v_fmamk_f32 v24, v24, 0x4038aa3b, v27
	v_add_f32_e32 v22, 1.0, v22
	v_fmamk_f32 v28, v28, 0x4038aa3b, v27
	v_rcp_f32_e32 v19, v19
	v_rcp_f32_e32 v18, v18
	v_exp_f32_e32 v21, v21
	v_exp_f32_e32 v25, v25
	v_mfma_f32_32x32x16_bf16 v[2:17], v[58:61], v[158:161], v[2:17]
	v_add_f32_e32 v23, 1.0, v23
	v_fmamk_f32 v32, v32, 0x4038aa3b, v27
	v_mul_f32_e32 v20, v20, v26
	v_mul_f32_e32 v24, v24, v30
	v_rcp_f32_e32 v22, v22
	v_rcp_f32_e32 v23, v23
	v_exp_f32_e32 v26, v29
	v_exp_f32_e32 v29, v33
	v_mfma_f32_32x32x16_bf16 v[2:17], v[54:57], v[154:157], v[2:17]
	v_mul_f32_e32 v28, v28, v31
	v_mul_f32_e32 v30, v32, v66
	v_fmac_f32_e32 v20, v19, v201
	v_fmac_f32_e32 v24, v18, v200
	v_fmac_f32_e32 v28, v22, v199
	v_fmac_f32_e32 v30, v23, v198
	v_mfma_f32_32x32x16_bf16 v[2:17], v[50:53], v[142:145], v[2:17]
	v_add_f32_e32 v18, 1.0, v21
	v_exp_f32_e32 v19, v20
	v_add_f32_e32 v20, 1.0, v25
	v_exp_f32_e32 v21, v24
	v_exp_f32_e32 v22, v28
	v_exp_f32_e32 v23, v30
	v_mfma_f32_32x32x16_bf16 v[2:17], v[46:49], v[130:133], v[2:17]
	v_add_f32_e32 v24, 1.0, v26
	v_add_f32_e32 v25, 1.0, v29
	v_fmac_f32_e32 v18, v18, v19
	v_fmac_f32_e32 v20, v20, v21
	v_fmac_f32_e32 v24, v24, v22
	v_fmac_f32_e32 v25, v25, v23
	v_mfma_f32_32x32x16_bf16 v[2:17], v[42:45], v[134:137], v[2:17]
	v_rcp_f32_e32 v18, v18
	v_rcp_f32_e32 v20, v20
	v_rcp_f32_e32 v24, v24
	v_rcp_f32_e32 v25, v25
	v_mfma_f32_32x32x16_bf16 v[2:17], v[38:41], v[138:141], v[2:17]
	v_fma_f32 v18, -v19, v18, v18
	v_fma_f32 v19, -v21, v20, v20
	v_fma_f32 v20, -v22, v24, v24
	v_fma_f32 v21, -v23, v25, v25
	v_mfma_f32_32x32x16_bf16 v[2:17], v[34:37], v[146:149], v[2:17]
	v_cvt_pk_bf16_f32 v18, v18, v19
	v_cvt_pk_bf16_f32 v19, v20, v21
	ds_write_b64 v211, v[18:19] offset:8192
	s_nop 9
	v_exp_f32_e32 v4, v4
	v_exp_f32_e32 v8, v8
	v_exp_f32_e32 v12, v12
	v_exp_f32_e32 v16, v16
	v_exp_f32_e32 v2, v2
	v_add_f32_e32 v18, 1.0, v4
	v_exp_f32_e32 v6, v6
	v_exp_f32_e32 v10, v10
	v_exp_f32_e32 v14, v14
	v_add_f32_e32 v19, 1.0, v8
	v_add_f32_e32 v20, 1.0, v12
	v_add_f32_e32 v21, 1.0, v16
	v_exp_f32_e32 v3, v3
	v_fmac_f32_e32 v18, v2, v18
	v_exp_f32_e32 v2, v7
	v_exp_f32_e32 v7, v11
	v_exp_f32_e32 v11, v15
	v_fmac_f32_e32 v19, v6, v19
	v_fmac_f32_e32 v20, v10, v20
	v_fmac_f32_e32 v21, v14, v21
	v_add_f32_e32 v3, 1.0, v3
	v_rcp_f32_e32 v6, v18
	v_rcp_f32_e32 v10, v19
	v_rcp_f32_e32 v14, v20
	v_rcp_f32_e32 v15, v21
	v_fmamk_f32 v4, v4, 0x4038aa3b, v27
	v_add_f32_e32 v2, 1.0, v2
	v_fmamk_f32 v8, v8, 0x4038aa3b, v27
	v_add_f32_e32 v7, 1.0, v7
	v_rcp_f32_e32 v3, v3
	v_rcp_f32_e32 v2, v2
	v_exp_f32_e32 v5, v5
	v_exp_f32_e32 v9, v9
	v_fmamk_f32 v12, v12, 0x4038aa3b, v27
	v_add_f32_e32 v11, 1.0, v11
	v_fmac_f32_e32 v27, 0x4038aa3b, v16
	v_mul_f32_e32 v4, v4, v6
	v_rcp_f32_e32 v6, v7
	v_rcp_f32_e32 v7, v11
	v_exp_f32_e32 v11, v13
	v_exp_f32_e32 v13, v17
	v_mul_f32_e32 v8, v8, v10
	v_mul_f32_e32 v10, v12, v14
	v_mul_f32_e32 v12, v27, v15
	v_fmac_f32_e32 v4, v3, v207
	v_fmac_f32_e32 v8, v2, v206
	v_fmac_f32_e32 v10, v6, v209
	v_fmac_f32_e32 v12, v7, v208
	v_add_f32_e32 v2, 1.0, v5
	v_exp_f32_e32 v3, v4
	v_exp_f32_e32 v4, v8
	v_exp_f32_e32 v5, v10
	v_exp_f32_e32 v6, v12
	v_add_f32_e32 v7, 1.0, v9
	v_add_f32_e32 v8, 1.0, v11
	v_add_f32_e32 v9, 1.0, v13
	v_fmac_f32_e32 v2, v2, v3
	v_fmac_f32_e32 v7, v7, v4
	v_fmac_f32_e32 v8, v8, v5
	v_fmac_f32_e32 v9, v9, v6
	v_rcp_f32_e32 v2, v2
	v_rcp_f32_e32 v7, v7
	v_rcp_f32_e32 v8, v8
	v_rcp_f32_e32 v9, v9
	v_fma_f32 v2, -v3, v2, v2
	v_fma_f32 v3, -v4, v7, v7
	v_fma_f32 v4, -v5, v8, v8
	v_fma_f32 v5, -v6, v9, v9
	v_cvt_pk_bf16_f32 v2, v2, v3
	v_cvt_pk_bf16_f32 v3, v4, v5
	ds_write_b64 v211, v[2:3] offset:8200
	s_waitcnt lgkmcnt(0)
	s_barrier

.Llight_path:
	s_waitcnt vmcnt(0)
	v_mul_u32_u24_e32 v236, 36, v228
	v_add_u32_e32 v236, v236, v230
	v_add_u32_e32 v237, s7, v229
	v_mul_u32_u24_e32 v238, 0x104, v228
	v_add_u32_e32 v238, v238, v237
	v_add_u32_e32 v238, 0xb840, v238
	ds_read_b128 v[2:5], v237 offset:36928
	ds_read_b128 v[6:9], v237 offset:36944
	ds_read_b128 v[10:13], v237 offset:36960
	ds_read_b128 v[14:17], v237 offset:36976
	ds_read_b128 v[18:21], v237 offset:37056
	ds_read_b128 v[22:25], v237 offset:37072
	ds_read_b128 v[26:29], v237 offset:37088
	ds_read_b128 v[30:33], v237 offset:37104
	ds_read_b128 v[162:165], v236 offset:16384
	ds_read_b128 v[166:169], v236 offset:16416
	ds_read_b128 v[170:173], v236 offset:16448
	ds_read_b128 v[174:177], v236 offset:16480
	s_waitcnt lgkmcnt(0)
	v_mfma_f32_32x32x16_bf16 v[2:17], v[94:97], v[162:165], v[2:17]
	v_mfma_f32_32x32x16_bf16 v[2:17], v[90:93], v[166:169], v[2:17]
	v_mfma_f32_32x32x16_bf16 v[2:17], v[86:89], v[170:173], v[2:17]
	v_mfma_f32_32x32x16_bf16 v[2:17], v[82:85], v[174:177], v[2:17]
	v_mfma_f32_32x32x16_bf16 v[18:33], v[46:49], v[162:165], v[18:33]
	ds_read_b128 v[130:133], v237 offset:36928
	ds_read_b128 v[134:137], v237 offset:36944
	ds_read_b128 v[138:141], v237 offset:36960
	v_mfma_f32_32x32x16_bf16 v[18:33], v[42:45], v[166:169], v[18:33]
	ds_read_b128 v[142:145], v237 offset:36976
	ds_read_b128 v[146:149], v237 offset:37056
	ds_read_b128 v[150:153], v237 offset:37072
	v_mfma_f32_32x32x16_bf16 v[18:33], v[38:41], v[170:173], v[18:33]
	ds_read_b128 v[154:157], v237 offset:37088
	ds_read_b128 v[158:161], v237 offset:37104
	ds_read_b128 v[178:181], v236 offset:20992
	v_mfma_f32_32x32x16_bf16 v[18:33], v[34:37], v[174:177], v[18:33]
	ds_read_b128 v[182:185], v236 offset:21024
	ds_read_b128 v[186:189], v236 offset:21056
	ds_read_b128 v[190:193], v236 offset:21088
	s_waitcnt lgkmcnt(0)
	v_mfma_f32_32x32x16_bf16 v[130:145], v[94:97], v[178:181], v[130:145]
	v_mfma_f32_32x32x16_bf16 v[130:145], v[90:93], v[182:185], v[130:145]
	v_mfma_f32_32x32x16_bf16 v[130:145], v[86:89], v[186:189], v[130:145]
	v_mfma_f32_32x32x16_bf16 v[130:145], v[82:85], v[190:193], v[130:145]
	s_nop 7
	ds_write_b128 v238, v[2:5] offset:0
	ds_write_b128 v238, v[6:9] offset:16
	ds_write_b128 v238, v[10:13] offset:32
	ds_write_b128 v238, v[14:17] offset:48
	ds_write_b128 v238, v[18:21] offset:128
	ds_write_b128 v238, v[22:25] offset:144
	ds_write_b128 v238, v[26:29] offset:160
	ds_write_b128 v238, v[30:33] offset:176
	v_mfma_f32_32x32x16_bf16 v[146:161], v[46:49], v[178:181], v[146:161]
	ds_read_b128 v[2:5], v237 offset:36928
	ds_read_b128 v[6:9], v237 offset:36944
	ds_read_b128 v[10:13], v237 offset:36960
	v_mfma_f32_32x32x16_bf16 v[146:161], v[42:45], v[182:185], v[146:161]
	ds_read_b128 v[14:17], v237 offset:36976
	ds_read_b128 v[18:21], v237 offset:37056
	ds_read_b128 v[22:25], v237 offset:37072
	v_mfma_f32_32x32x16_bf16 v[146:161], v[38:41], v[186:189], v[146:161]
	ds_read_b128 v[26:29], v237 offset:37088
	ds_read_b128 v[30:33], v237 offset:37104
	ds_read_b128 v[162:165], v236 offset:25600
	v_mfma_f32_32x32x16_bf16 v[146:161], v[34:37], v[190:193], v[146:161]
	ds_read_b128 v[166:169], v236 offset:25632
	ds_read_b128 v[170:173], v236 offset:25664
	ds_read_b128 v[174:177], v236 offset:25696
	s_waitcnt lgkmcnt(0)
	v_mfma_f32_32x32x16_bf16 v[2:17], v[94:97], v[162:165], v[2:17]
	v_mfma_f32_32x32x16_bf16 v[2:17], v[90:93], v[166:169], v[2:17]
	v_mfma_f32_32x32x16_bf16 v[2:17], v[86:89], v[170:173], v[2:17]
	v_mfma_f32_32x32x16_bf16 v[2:17], v[82:85], v[174:177], v[2:17]
	s_nop 7
	v_add_u32_e32 v239, 0x8200, v238
	ds_write_b128 v239, v[130:133] offset:0
	ds_write_b128 v239, v[134:137] offset:16
	ds_write_b128 v239, v[138:141] offset:32
	ds_write_b128 v239, v[142:145] offset:48
	ds_write_b128 v239, v[146:149] offset:128
	ds_write_b128 v239, v[150:153] offset:144
	ds_write_b128 v239, v[154:157] offset:160
	ds_write_b128 v239, v[158:161] offset:176
	v_mfma_f32_32x32x16_bf16 v[18:33], v[46:49], v[162:165], v[18:33]
	ds_read_b128 v[130:133], v237 offset:36928
	ds_read_b128 v[134:137], v237 offset:36944
	ds_read_b128 v[138:141], v237 offset:36960
	v_mfma_f32_32x32x16_bf16 v[18:33], v[42:45], v[166:169], v[18:33]
	ds_read_b128 v[142:145], v237 offset:36976
	ds_read_b128 v[146:149], v237 offset:37056
	ds_read_b128 v[150:153], v237 offset:37072
	v_mfma_f32_32x32x16_bf16 v[18:33], v[38:41], v[170:173], v[18:33]
	ds_read_b128 v[154:157], v237 offset:37088
	ds_read_b128 v[158:161], v237 offset:37104
	ds_read_b128 v[178:181], v236 offset:30208
	v_mfma_f32_32x32x16_bf16 v[18:33], v[34:37], v[174:177], v[18:33]
	ds_read_b128 v[182:185], v236 offset:30240
	ds_read_b128 v[186:189], v236 offset:30272
	ds_read_b128 v[190:193], v236 offset:30304
	s_waitcnt lgkmcnt(0)
	v_mfma_f32_32x32x16_bf16 v[130:145], v[94:97], v[178:181], v[130:145]
	v_mfma_f32_32x32x16_bf16 v[130:145], v[90:93], v[182:185], v[130:145]
	v_mfma_f32_32x32x16_bf16 v[130:145], v[86:89], v[186:189], v[130:145]
	v_mfma_f32_32x32x16_bf16 v[130:145], v[82:85], v[190:193], v[130:145]
	s_nop 7
	v_add_u32_e32 v239, 0x10400, v238
	ds_write_b128 v239, v[2:5] offset:0
	ds_write_b128 v239, v[6:9] offset:16
	ds_write_b128 v239, v[10:13] offset:32
	ds_write_b128 v239, v[14:17] offset:48
	ds_write_b128 v239, v[18:21] offset:128
	ds_write_b128 v239, v[22:25] offset:144
	ds_write_b128 v239, v[26:29] offset:160
	ds_write_b128 v239, v[30:33] offset:176
	v_mfma_f32_32x32x16_bf16 v[146:161], v[46:49], v[178:181], v[146:161]
	v_mfma_f32_32x32x16_bf16 v[146:161], v[42:45], v[182:185], v[146:161]
	v_mfma_f32_32x32x16_bf16 v[146:161], v[38:41], v[186:189], v[146:161]
	v_mfma_f32_32x32x16_bf16 v[146:161], v[34:37], v[190:193], v[146:161]
	s_nop 7
	s_nop 7
	v_cmp_gt_u32_e32 vcc, 16, v228
	s_and_saveexec_b64 s[20:21], vcc
	v_add_u32_e32 v239, 0x18600, v238
	ds_write_b128 v239, v[130:133] offset:0
	ds_write_b128 v239, v[134:137] offset:16
	ds_write_b128 v239, v[138:141] offset:32
	ds_write_b128 v239, v[142:145] offset:48
	ds_write_b128 v239, v[146:149] offset:128
	ds_write_b128 v239, v[150:153] offset:144
	ds_write_b128 v239, v[154:157] offset:160
	ds_write_b128 v239, v[158:161] offset:176
	s_or_b64 exec, exec, s[20:21]
	s_waitcnt vmcnt(0) lgkmcnt(0)
	s_nop 7
	s_nop 7
	v_add_u32_e32 v231, s7, v229
	v_add_u32_e32 v231, 0xb840, v231
	v_add_u32_e32 v211, s6, v210
	s_mov_b32 s12, 0x4038aa3b
	v_mov_b32_e32 v235, 0xc038aa3b
	s_nop 0
	s_load_dwordx8 s[4:11], s[0:1], 0x10
	s_waitcnt lgkmcnt(0)
	v_add_u32_e32 v232, 0x24e80, v228
	ds_read_b32 v244, v232
	ds_read_b32 v245, v232 offset:128
	v_mov_b32_e32 v194, 0
	v_mov_b32_e32 v195, 0
	v_mov_b32_e32 v196, 0
	v_mov_b32_e32 v197, 0
	v_mov_b32_e32 v198, 0
	v_mov_b32_e32 v199, 0
	v_mov_b32_e32 v200, 0
	v_mov_b32_e32 v201, 0
	v_mov_b32_e32 v202, 0
	v_mov_b32_e32 v203, 0
	v_mov_b32_e32 v204, 0
	v_mov_b32_e32 v205, 0
	v_mov_b32_e32 v206, 0
	v_mov_b32_e32 v207, 0
	v_mov_b32_e32 v208, 0
	v_mov_b32_e32 v209, 0
	v_add_u32_e32 v232, 0x100, v232
	s_waitcnt lgkmcnt(0)
	v_add_u32_e32 v233, v231, v244
	v_add_u32_e32 v234, v231, v245
	ds_read_b128 v[2:5], v233 offset:0
	ds_read_b128 v[6:9], v233 offset:16
	ds_read_b128 v[10:13], v233 offset:32
	ds_read_b128 v[14:17], v233 offset:48
	ds_read_b128 v[18:21], v233 offset:128
	ds_read_b128 v[22:25], v233 offset:144
	ds_read_b128 v[26:29], v233 offset:160
	ds_read_b128 v[30:33], v233 offset:176
	ds_read_b128 v[34:37], v234 offset:0
	ds_read_b128 v[38:41], v234 offset:16
	ds_read_b128 v[42:45], v234 offset:32
	ds_read_b128 v[46:49], v234 offset:48
	s_movk_i32 s16, 18
	s_waitcnt lgkmcnt(0)
	ds_read_b128 v[82:85], v234 offset:128
	ds_read_b128 v[86:89], v234 offset:144
	ds_read_b128 v[90:93], v234 offset:160
	ds_read_b128 v[94:97], v234 offset:176
	ds_read_b32 v244, v232 offset:0
	v_exp_f32_e32 v212, v4
	v_exp_f32_e32 v213, v8
	v_exp_f32_e32 v214, v12
	v_exp_f32_e32 v215, v16
	v_exp_f32_e32 v216, v2
	v_exp_f32_e32 v217, v6
	v_exp_f32_e32 v218, v10
	v_exp_f32_e32 v219, v14
	v_add_f32_e32 v236, 1.0, v212
	v_add_f32_e32 v237, 1.0, v213
	v_add_f32_e32 v238, 1.0, v214
	v_add_f32_e32 v239, 1.0, v215
	v_fma_f32 v240, v212, s12, v235
	v_fma_f32 v241, v213, s12, v235
	v_fma_f32 v242, v214, s12, v235
	v_fma_f32 v243, v215, s12, v235
	v_fmac_f32_e32 v236, v216, v236
	v_fmac_f32_e32 v237, v217, v237
	v_fmac_f32_e32 v238, v218, v238
	v_fmac_f32_e32 v239, v219, v239
	v_rcp_f32_e32 v216, v236
	v_rcp_f32_e32 v217, v237
	v_rcp_f32_e32 v218, v238
	v_rcp_f32_e32 v219, v239
	v_exp_f32_e32 v224, v5
	v_exp_f32_e32 v225, v9
	v_exp_f32_e32 v226, v13
	v_exp_f32_e32 v227, v17
	v_mul_f32_e32 v194, v240, v216
	v_mul_f32_e32 v195, v241, v217
	v_mul_f32_e32 v196, v242, v218
	v_mul_f32_e32 v197, v243, v219
	v_exp_f32_e32 v212, v194
	v_exp_f32_e32 v213, v195
	v_exp_f32_e32 v214, v196
	v_exp_f32_e32 v215, v197
	v_add_f32_e32 v224, 1.0, v224
	v_add_f32_e32 v225, 1.0, v225
	v_add_f32_e32 v226, 1.0, v226
	v_add_f32_e32 v227, 1.0, v227
	v_fmac_f32_e32 v224, v224, v212
	v_fmac_f32_e32 v225, v225, v213
	v_fmac_f32_e32 v226, v226, v214
	v_fmac_f32_e32 v227, v227, v215
	v_rcp_f32_e32 v224, v224
	v_rcp_f32_e32 v225, v225
	v_rcp_f32_e32 v226, v226
	v_rcp_f32_e32 v227, v227
	v_fma_f32 v224, -v212, v224, v224
	v_fma_f32 v225, -v213, v225, v225
	v_fma_f32 v226, -v214, v226, v226
	v_fma_f32 v227, -v215, v227, v227
	v_cvt_pk_bf16_f32 v224, v224, v225
	v_cvt_pk_bf16_f32 v225, v226, v227
	ds_write_b64 v211, v[224:225] offset:0
	s_waitcnt lgkmcnt(1)
	v_add_u32_e32 v233, v231, v244
	ds_read_b128 v[2:5], v233 offset:0
	ds_read_b128 v[6:9], v233 offset:16
	ds_read_b128 v[10:13], v233 offset:32
	ds_read_b128 v[14:17], v233 offset:48
	v_exp_f32_e32 v212, v20
	v_exp_f32_e32 v213, v24
	v_exp_f32_e32 v214, v28
	v_exp_f32_e32 v215, v32
	v_exp_f32_e32 v216, v18
	v_exp_f32_e32 v217, v22
	v_exp_f32_e32 v218, v26
	v_exp_f32_e32 v219, v30
	v_add_f32_e32 v236, 1.0, v212
	v_add_f32_e32 v237, 1.0, v213
	v_add_f32_e32 v238, 1.0, v214
	v_add_f32_e32 v239, 1.0, v215
	v_fma_f32 v240, v212, s12, v235
	v_fma_f32 v241, v213, s12, v235
	v_fma_f32 v242, v214, s12, v235
	v_fma_f32 v243, v215, s12, v235
	v_fmac_f32_e32 v236, v216, v236
	v_fmac_f32_e32 v237, v217, v237
	v_fmac_f32_e32 v238, v218, v238
	v_fmac_f32_e32 v239, v219, v239
	v_rcp_f32_e32 v216, v236
	v_rcp_f32_e32 v217, v237
	v_rcp_f32_e32 v218, v238
	v_rcp_f32_e32 v219, v239
	v_exp_f32_e32 v224, v21
	v_exp_f32_e32 v225, v25
	v_exp_f32_e32 v226, v29
	v_exp_f32_e32 v227, v33
	v_mul_f32_e32 v198, v240, v216
	v_mul_f32_e32 v199, v241, v217
	v_mul_f32_e32 v200, v242, v218
	v_mul_f32_e32 v201, v243, v219
	v_exp_f32_e32 v212, v198
	v_exp_f32_e32 v213, v199
	v_exp_f32_e32 v214, v200
	v_exp_f32_e32 v215, v201
	v_add_f32_e32 v224, 1.0, v224
	v_add_f32_e32 v225, 1.0, v225
	v_add_f32_e32 v226, 1.0, v226
	v_add_f32_e32 v227, 1.0, v227
	v_fmac_f32_e32 v224, v224, v212
	v_fmac_f32_e32 v225, v225, v213
	v_fmac_f32_e32 v226, v226, v214
	v_fmac_f32_e32 v227, v227, v215
	v_rcp_f32_e32 v224, v224
	v_rcp_f32_e32 v225, v225
	v_rcp_f32_e32 v226, v226
	v_rcp_f32_e32 v227, v227
	v_fma_f32 v224, -v212, v224, v224
	v_fma_f32 v225, -v213, v225, v225
	v_fma_f32 v226, -v214, v226, v226
	v_fma_f32 v227, -v215, v227, v227
	v_cvt_pk_bf16_f32 v224, v224, v225
	v_cvt_pk_bf16_f32 v225, v226, v227
	ds_write_b64 v211, v[224:225] offset:8
	s_waitcnt lgkmcnt(0)
	s_barrier
	ds_read_b128 v[130:133], v210 offset:0
	ds_read_b128 v[134:137], v210 offset:1024
	ds_read_b128 v[18:21], v233 offset:128
	ds_read_b128 v[22:25], v233 offset:144
	ds_read_b128 v[26:29], v233 offset:160
	ds_read_b128 v[30:33], v233 offset:176
	ds_read_b32 v245, v232 offset:128
	v_exp_f32_e32 v212, v36
	v_exp_f32_e32 v213, v40
	v_exp_f32_e32 v214, v44
	v_exp_f32_e32 v215, v48
	ds_read_b128 v[138:141], v210 offset:2048
	ds_read_b128 v[142:145], v210 offset:3072
	v_exp_f32_e32 v216, v34
	v_exp_f32_e32 v217, v38
	v_exp_f32_e32 v218, v42
	v_exp_f32_e32 v219, v46
	v_add_f32_e32 v236, 1.0, v212
	v_add_f32_e32 v237, 1.0, v213
	v_add_f32_e32 v238, 1.0, v214
	v_add_f32_e32 v239, 1.0, v215
	v_fma_f32 v240, v212, s12, v235
	v_fma_f32 v241, v213, s12, v235
	v_fma_f32 v242, v214, s12, v235
	v_fma_f32 v243, v215, s12, v235
	ds_read_b128 v[146:149], v210 offset:4096
	ds_read_b128 v[150:153], v210 offset:5120
	v_fmac_f32_e32 v236, v216, v236
	v_fmac_f32_e32 v237, v217, v237
	v_fmac_f32_e32 v238, v218, v238
	v_fmac_f32_e32 v239, v219, v239
	ds_read_b128 v[154:157], v210 offset:6144
	ds_read_b128 v[158:161], v210 offset:7168
	v_rcp_f32_e32 v216, v236
	v_rcp_f32_e32 v217, v237
	v_rcp_f32_e32 v218, v238
	v_rcp_f32_e32 v219, v239
	v_exp_f32_e32 v224, v37
	v_exp_f32_e32 v225, v41
	v_exp_f32_e32 v226, v45
	v_exp_f32_e32 v227, v49
	v_mul_f32_e32 v202, v240, v216
	v_mul_f32_e32 v203, v241, v217
	v_mul_f32_e32 v204, v242, v218
	v_mul_f32_e32 v205, v243, v219
	v_exp_f32_e32 v212, v202
	v_exp_f32_e32 v213, v203
	v_exp_f32_e32 v214, v204
	v_exp_f32_e32 v215, v205
	v_add_f32_e32 v224, 1.0, v224
	v_add_f32_e32 v225, 1.0, v225
	v_add_f32_e32 v226, 1.0, v226
	v_add_f32_e32 v227, 1.0, v227
	v_fmac_f32_e32 v224, v224, v212
	v_fmac_f32_e32 v225, v225, v213
	v_fmac_f32_e32 v226, v226, v214
	v_fmac_f32_e32 v227, v227, v215
	v_rcp_f32_e32 v224, v224
	v_rcp_f32_e32 v225, v225
	v_rcp_f32_e32 v226, v226
	v_rcp_f32_e32 v227, v227
	v_fma_f32 v224, -v212, v224, v224
	v_fma_f32 v225, -v213, v225, v225
	v_fma_f32 v226, -v214, v226, v226
	v_fma_f32 v227, -v215, v227, v227
	v_cvt_pk_bf16_f32 v224, v224, v225
	v_cvt_pk_bf16_f32 v225, v226, v227
	ds_write_b64 v211, v[224:225] offset:8192
	s_waitcnt lgkmcnt(1)
	v_mfma_f32_32x32x16_bf16 v[2:17], v[126:129], v[130:133], v[2:17]
	v_add_u32_e32 v234, v231, v245
	ds_read_b128 v[34:37], v234 offset:0
	ds_read_b128 v[38:41], v234 offset:16
	ds_read_b128 v[42:45], v234 offset:32
	ds_read_b128 v[46:49], v234 offset:48
	v_add_u32_e32 v232, 0x100, v232
	v_exp_f32_e32 v212, v84
	v_exp_f32_e32 v213, v88
	v_exp_f32_e32 v214, v92
	v_exp_f32_e32 v215, v96
	v_mfma_f32_32x32x16_bf16 v[2:17], v[122:125], v[134:137], v[2:17]
	v_exp_f32_e32 v216, v82
	v_exp_f32_e32 v217, v86
	v_exp_f32_e32 v218, v90
	v_exp_f32_e32 v219, v94
	v_add_f32_e32 v236, 1.0, v212
	v_add_f32_e32 v237, 1.0, v213
	v_add_f32_e32 v238, 1.0, v214
	v_add_f32_e32 v239, 1.0, v215
	v_fma_f32 v240, v212, s12, v235
	v_fma_f32 v241, v213, s12, v235
	v_fma_f32 v242, v214, s12, v235
	v_fma_f32 v243, v215, s12, v235
	v_mfma_f32_32x32x16_bf16 v[2:17], v[118:121], v[138:141], v[2:17]
	v_fmac_f32_e32 v236, v216, v236
	v_fmac_f32_e32 v237, v217, v237
	v_fmac_f32_e32 v238, v218, v238
	v_fmac_f32_e32 v239, v219, v239
	v_mfma_f32_32x32x16_bf16 v[2:17], v[114:117], v[142:145], v[2:17]
	v_rcp_f32_e32 v216, v236
	v_rcp_f32_e32 v217, v237
	v_rcp_f32_e32 v218, v238
	v_rcp_f32_e32 v219, v239
	v_mfma_f32_32x32x16_bf16 v[2:17], v[110:113], v[146:149], v[2:17]
	v_exp_f32_e32 v224, v85
	v_exp_f32_e32 v225, v89
	v_exp_f32_e32 v226, v93
	v_exp_f32_e32 v227, v97
	v_mul_f32_e32 v206, v240, v216
	v_mul_f32_e32 v207, v241, v217
	v_mul_f32_e32 v208, v242, v218
	v_mul_f32_e32 v209, v243, v219
	v_mfma_f32_32x32x16_bf16 v[2:17], v[106:109], v[150:153], v[2:17]
	v_mfma_f32_32x32x16_bf16 v[2:17], v[102:105], v[154:157], v[2:17]
	v_exp_f32_e32 v212, v206
	v_exp_f32_e32 v213, v207
	v_exp_f32_e32 v214, v208
	v_exp_f32_e32 v215, v209
	v_add_f32_e32 v224, 1.0, v224
	v_add_f32_e32 v225, 1.0, v225
	v_add_f32_e32 v226, 1.0, v226
	v_add_f32_e32 v227, 1.0, v227
	v_fmac_f32_e32 v224, v224, v212
	v_fmac_f32_e32 v225, v225, v213
	v_fmac_f32_e32 v226, v226, v214
	v_fmac_f32_e32 v227, v227, v215
	v_mfma_f32_32x32x16_bf16 v[2:17], v[98:101], v[158:161], v[2:17]
	v_rcp_f32_e32 v224, v224
	v_rcp_f32_e32 v225, v225
	v_rcp_f32_e32 v226, v226
	v_rcp_f32_e32 v227, v227
	v_fma_f32 v224, -v212, v224, v224
	v_fma_f32 v225, -v213, v225, v225
	v_fma_f32 v226, -v214, v226, v226
	v_fma_f32 v227, -v215, v227, v227
	v_cvt_pk_bf16_f32 v224, v224, v225
	v_cvt_pk_bf16_f32 v225, v226, v227
	ds_write_b64 v211, v[224:225] offset:8200
	s_waitcnt lgkmcnt(0)
	s_barrier
.Llight_loop:
	v_mfma_f32_32x32x16_bf16 v[18:33], v[78:81], v[130:133], v[18:33]
	ds_read_b128 v[162:165], v210 offset:8192
	ds_read_b128 v[166:169], v210 offset:9216
	ds_read_b128 v[82:85], v234 offset:128
	ds_read_b128 v[86:89], v234 offset:144
	ds_read_b128 v[90:93], v234 offset:160
	ds_read_b128 v[94:97], v234 offset:176
	ds_read_b32 v244, v232 offset:0
	v_exp_f32_e32 v212, v4
	v_exp_f32_e32 v213, v8
	v_exp_f32_e32 v214, v12
	v_exp_f32_e32 v215, v16
	v_mfma_f32_32x32x16_bf16 v[18:33], v[74:77], v[134:137], v[18:33]
	ds_read_b128 v[170:173], v210 offset:10240
	ds_read_b128 v[174:177], v210 offset:11264
	v_exp_f32_e32 v216, v2
	v_exp_f32_e32 v217, v6
	v_exp_f32_e32 v218, v10
	v_exp_f32_e32 v219, v14
	v_add_f32_e32 v236, 1.0, v212
	v_add_f32_e32 v237, 1.0, v213
	v_add_f32_e32 v238, 1.0, v214
	v_add_f32_e32 v239, 1.0, v215
	v_fma_f32 v240, v212, s12, v235
	v_fma_f32 v241, v213, s12, v235
	v_fma_f32 v242, v214, s12, v235
	v_fma_f32 v243, v215, s12, v235
	v_mfma_f32_32x32x16_bf16 v[18:33], v[70:73], v[138:141], v[18:33]
	ds_read_b128 v[178:181], v210 offset:12288
	ds_read_b128 v[182:185], v210 offset:13312
	v_exp_f32_e32 v220, v3
	v_exp_f32_e32 v221, v7
	v_exp_f32_e32 v222, v11
	v_exp_f32_e32 v223, v15
	v_fmac_f32_e32 v236, v216, v236
	v_fmac_f32_e32 v237, v217, v237
	v_fmac_f32_e32 v238, v218, v238
	v_fmac_f32_e32 v239, v219, v239
	v_mfma_f32_32x32x16_bf16 v[18:33], v[66:69], v[142:145], v[18:33]
	ds_read_b128 v[186:189], v210 offset:14336
	ds_read_b128 v[190:193], v210 offset:15360
	v_rcp_f32_e32 v216, v236
	v_rcp_f32_e32 v217, v237
	v_rcp_f32_e32 v218, v238
	v_rcp_f32_e32 v219, v239
	v_add_f32_e32 v220, 1.0, v220
	v_add_f32_e32 v221, 1.0, v221
	v_add_f32_e32 v222, 1.0, v222
	v_add_f32_e32 v223, 1.0, v223
	v_mfma_f32_32x32x16_bf16 v[18:33], v[62:65], v[146:149], v[18:33]
	v_rcp_f32_e32 v220, v220
	v_rcp_f32_e32 v221, v221
	v_rcp_f32_e32 v222, v222
	v_rcp_f32_e32 v223, v223
	v_mul_f32_e32 v240, v240, v216
	v_mul_f32_e32 v241, v241, v217
	v_mul_f32_e32 v242, v242, v218
	v_mul_f32_e32 v243, v243, v219
	v_mfma_f32_32x32x16_bf16 v[18:33], v[58:61], v[150:153], v[18:33]
	v_exp_f32_e32 v224, v5
	v_exp_f32_e32 v225, v9
	v_exp_f32_e32 v226, v13
	v_exp_f32_e32 v227, v17
	v_fma_f32 v194, v220, v194, v240
	v_fma_f32 v195, v221, v195, v241
	v_fma_f32 v196, v222, v196, v242
	v_fma_f32 v197, v223, v197, v243
	v_mfma_f32_32x32x16_bf16 v[18:33], v[54:57], v[154:157], v[18:33]
	v_exp_f32_e32 v212, v194
	v_exp_f32_e32 v213, v195
	v_exp_f32_e32 v214, v196
	v_exp_f32_e32 v215, v197
	v_add_f32_e32 v224, 1.0, v224
	v_add_f32_e32 v225, 1.0, v225
	v_add_f32_e32 v226, 1.0, v226
	v_add_f32_e32 v227, 1.0, v227
	v_fmac_f32_e32 v224, v224, v212
	v_fmac_f32_e32 v225, v225, v213
	v_fmac_f32_e32 v226, v226, v214
	v_fmac_f32_e32 v227, v227, v215
	v_mfma_f32_32x32x16_bf16 v[18:33], v[50:53], v[158:161], v[18:33]
	v_rcp_f32_e32 v224, v224
	v_rcp_f32_e32 v225, v225
	v_rcp_f32_e32 v226, v226
	v_rcp_f32_e32 v227, v227
	v_fma_f32 v224, -v212, v224, v224
	v_fma_f32 v225, -v213, v225, v225
	v_fma_f32 v226, -v214, v226, v226
	v_fma_f32 v227, -v215, v227, v227
	v_cvt_pk_bf16_f32 v224, v224, v225
	v_cvt_pk_bf16_f32 v225, v226, v227
	ds_write_b64 v211, v[224:225] offset:0
	s_waitcnt lgkmcnt(1)
	v_mfma_f32_32x32x16_bf16 v[34:49], v[126:129], v[162:165], v[34:49]
	v_add_u32_e32 v233, v231, v244
	ds_read_b128 v[2:5], v233 offset:0
	ds_read_b128 v[6:9], v233 offset:16
	ds_read_b128 v[10:13], v233 offset:32
	ds_read_b128 v[14:17], v233 offset:48
	v_exp_f32_e32 v212, v20
	v_exp_f32_e32 v213, v24
	v_exp_f32_e32 v214, v28
	v_exp_f32_e32 v215, v32
	v_mfma_f32_32x32x16_bf16 v[34:49], v[122:125], v[166:169], v[34:49]
	v_exp_f32_e32 v216, v18
	v_exp_f32_e32 v217, v22
	v_exp_f32_e32 v218, v26
	v_exp_f32_e32 v219, v30
	v_add_f32_e32 v236, 1.0, v212
	v_add_f32_e32 v237, 1.0, v213
	v_add_f32_e32 v238, 1.0, v214
	v_add_f32_e32 v239, 1.0, v215
	v_fma_f32 v240, v212, s12, v235
	v_fma_f32 v241, v213, s12, v235
	v_fma_f32 v242, v214, s12, v235
	v_fma_f32 v243, v215, s12, v235
	v_mfma_f32_32x32x16_bf16 v[34:49], v[118:121], v[170:173], v[34:49]
	v_exp_f32_e32 v220, v19
	v_exp_f32_e32 v221, v23
	v_exp_f32_e32 v222, v27
	v_exp_f32_e32 v223, v31
	v_fmac_f32_e32 v236, v216, v236
	v_fmac_f32_e32 v237, v217, v237
	v_fmac_f32_e32 v238, v218, v238
	v_fmac_f32_e32 v239, v219, v239
	v_mfma_f32_32x32x16_bf16 v[34:49], v[114:117], v[174:177], v[34:49]
	v_rcp_f32_e32 v216, v236
	v_rcp_f32_e32 v217, v237
	v_rcp_f32_e32 v218, v238
	v_rcp_f32_e32 v219, v239
	v_add_f32_e32 v220, 1.0, v220
	v_add_f32_e32 v221, 1.0, v221
	v_add_f32_e32 v222, 1.0, v222
	v_add_f32_e32 v223, 1.0, v223
	v_mfma_f32_32x32x16_bf16 v[34:49], v[110:113], v[178:181], v[34:49]
	v_rcp_f32_e32 v220, v220
	v_rcp_f32_e32 v221, v221
	v_rcp_f32_e32 v222, v222
	v_rcp_f32_e32 v223, v223
	v_mul_f32_e32 v240, v240, v216
	v_mul_f32_e32 v241, v241, v217
	v_mul_f32_e32 v242, v242, v218
	v_mul_f32_e32 v243, v243, v219
	v_mfma_f32_32x32x16_bf16 v[34:49], v[106:109], v[182:185], v[34:49]
	v_exp_f32_e32 v224, v21
	v_exp_f32_e32 v225, v25
	v_exp_f32_e32 v226, v29
	v_exp_f32_e32 v227, v33
	v_fma_f32 v198, v220, v198, v240
	v_fma_f32 v199, v221, v199, v241
	v_fma_f32 v200, v222, v200, v242
	v_fma_f32 v201, v223, v201, v243
	v_mfma_f32_32x32x16_bf16 v[34:49], v[102:105], v[186:189], v[34:49]
	v_exp_f32_e32 v212, v198
	v_exp_f32_e32 v213, v199
	v_exp_f32_e32 v214, v200
	v_exp_f32_e32 v215, v201
	v_add_f32_e32 v224, 1.0, v224
	v_add_f32_e32 v225, 1.0, v225
	v_add_f32_e32 v226, 1.0, v226
	v_add_f32_e32 v227, 1.0, v227
	v_fmac_f32_e32 v224, v224, v212
	v_fmac_f32_e32 v225, v225, v213
	v_fmac_f32_e32 v226, v226, v214
	v_fmac_f32_e32 v227, v227, v215
	v_mfma_f32_32x32x16_bf16 v[34:49], v[98:101], v[190:193], v[34:49]
	v_rcp_f32_e32 v224, v224
	v_rcp_f32_e32 v225, v225
	v_rcp_f32_e32 v226, v226
	v_rcp_f32_e32 v227, v227
	v_fma_f32 v224, -v212, v224, v224
	v_fma_f32 v225, -v213, v225, v225
	v_fma_f32 v226, -v214, v226, v226
	v_fma_f32 v227, -v215, v227, v227
	v_cvt_pk_bf16_f32 v224, v224, v225
	v_cvt_pk_bf16_f32 v225, v226, v227
	ds_write_b64 v211, v[224:225] offset:8
	s_waitcnt lgkmcnt(0)
	s_barrier
	v_mfma_f32_32x32x16_bf16 v[82:97], v[78:81], v[162:165], v[82:97]
	ds_read_b128 v[130:133], v210 offset:0
	ds_read_b128 v[134:137], v210 offset:1024
	ds_read_b128 v[18:21], v233 offset:128
	ds_read_b128 v[22:25], v233 offset:144
	ds_read_b128 v[26:29], v233 offset:160
	ds_read_b128 v[30:33], v233 offset:176
	ds_read_b32 v245, v232 offset:128
	v_exp_f32_e32 v212, v36
	v_exp_f32_e32 v213, v40
	v_exp_f32_e32 v214, v44
	v_exp_f32_e32 v215, v48
	v_mfma_f32_32x32x16_bf16 v[82:97], v[74:77], v[166:169], v[82:97]
	ds_read_b128 v[138:141], v210 offset:2048
	ds_read_b128 v[142:145], v210 offset:3072
	v_exp_f32_e32 v216, v34
	v_exp_f32_e32 v217, v38
	v_exp_f32_e32 v218, v42
	v_exp_f32_e32 v219, v46
	v_add_f32_e32 v236, 1.0, v212
	v_add_f32_e32 v237, 1.0, v213
	v_add_f32_e32 v238, 1.0, v214
	v_add_f32_e32 v239, 1.0, v215
	v_fma_f32 v240, v212, s12, v235
	v_fma_f32 v241, v213, s12, v235
	v_fma_f32 v242, v214, s12, v235
	v_fma_f32 v243, v215, s12, v235
	v_mfma_f32_32x32x16_bf16 v[82:97], v[70:73], v[170:173], v[82:97]
	ds_read_b128 v[146:149], v210 offset:4096
	ds_read_b128 v[150:153], v210 offset:5120
	v_exp_f32_e32 v220, v35
	v_exp_f32_e32 v221, v39
	v_exp_f32_e32 v222, v43
	v_exp_f32_e32 v223, v47
	v_fmac_f32_e32 v236, v216, v236
	v_fmac_f32_e32 v237, v217, v237
	v_fmac_f32_e32 v238, v218, v238
	v_fmac_f32_e32 v239, v219, v239
	v_mfma_f32_32x32x16_bf16 v[82:97], v[66:69], v[174:177], v[82:97]
	ds_read_b128 v[154:157], v210 offset:6144
	ds_read_b128 v[158:161], v210 offset:7168
	v_rcp_f32_e32 v216, v236
	v_rcp_f32_e32 v217, v237
	v_rcp_f32_e32 v218, v238
	v_rcp_f32_e32 v219, v239
	v_add_f32_e32 v220, 1.0, v220
	v_add_f32_e32 v221, 1.0, v221
	v_add_f32_e32 v222, 1.0, v222
	v_add_f32_e32 v223, 1.0, v223
	v_mfma_f32_32x32x16_bf16 v[82:97], v[62:65], v[178:181], v[82:97]
	v_rcp_f32_e32 v220, v220
	v_rcp_f32_e32 v221, v221
	v_rcp_f32_e32 v222, v222
	v_rcp_f32_e32 v223, v223
	v_mul_f32_e32 v240, v240, v216
	v_mul_f32_e32 v241, v241, v217
	v_mul_f32_e32 v242, v242, v218
	v_mul_f32_e32 v243, v243, v219
	v_mfma_f32_32x32x16_bf16 v[82:97], v[58:61], v[182:185], v[82:97]
	v_exp_f32_e32 v224, v37
	v_exp_f32_e32 v225, v41
	v_exp_f32_e32 v226, v45
	v_exp_f32_e32 v227, v49
	v_fma_f32 v202, v220, v202, v240
	v_fma_f32 v203, v221, v203, v241
	v_fma_f32 v204, v222, v204, v242
	v_fma_f32 v205, v223, v205, v243
	v_mfma_f32_32x32x16_bf16 v[82:97], v[54:57], v[186:189], v[82:97]
	v_exp_f32_e32 v212, v202
	v_exp_f32_e32 v213, v203
	v_exp_f32_e32 v214, v204
	v_exp_f32_e32 v215, v205
	v_add_f32_e32 v224, 1.0, v224
	v_add_f32_e32 v225, 1.0, v225
	v_add_f32_e32 v226, 1.0, v226
	v_add_f32_e32 v227, 1.0, v227
	v_fmac_f32_e32 v224, v224, v212
	v_fmac_f32_e32 v225, v225, v213
	v_fmac_f32_e32 v226, v226, v214
	v_fmac_f32_e32 v227, v227, v215
	v_mfma_f32_32x32x16_bf16 v[82:97], v[50:53], v[190:193], v[82:97]
	v_rcp_f32_e32 v224, v224
	v_rcp_f32_e32 v225, v225
	v_rcp_f32_e32 v226, v226
	v_rcp_f32_e32 v227, v227
	v_fma_f32 v224, -v212, v224, v224
	v_fma_f32 v225, -v213, v225, v225
	v_fma_f32 v226, -v214, v226, v226
	v_fma_f32 v227, -v215, v227, v227
	v_cvt_pk_bf16_f32 v224, v224, v225
	v_cvt_pk_bf16_f32 v225, v226, v227
	ds_write_b64 v211, v[224:225] offset:8192
	s_waitcnt lgkmcnt(1)
	v_mfma_f32_32x32x16_bf16 v[2:17], v[126:129], v[130:133], v[2:17]
	v_add_u32_e32 v234, v231, v245
	ds_read_b128 v[34:37], v234 offset:0
	ds_read_b128 v[38:41], v234 offset:16
	ds_read_b128 v[42:45], v234 offset:32
	ds_read_b128 v[46:49], v234 offset:48
	v_add_u32_e32 v232, 0x100, v232
	v_exp_f32_e32 v212, v84
	v_exp_f32_e32 v213, v88
	v_exp_f32_e32 v214, v92
	v_exp_f32_e32 v215, v96
	v_mfma_f32_32x32x16_bf16 v[2:17], v[122:125], v[134:137], v[2:17]
	v_exp_f32_e32 v216, v82
	v_exp_f32_e32 v217, v86
	v_exp_f32_e32 v218, v90
	v_exp_f32_e32 v219, v94
	v_add_f32_e32 v236, 1.0, v212
	v_add_f32_e32 v237, 1.0, v213
	v_add_f32_e32 v238, 1.0, v214
	v_add_f32_e32 v239, 1.0, v215
	v_fma_f32 v240, v212, s12, v235
	v_fma_f32 v241, v213, s12, v235
	v_fma_f32 v242, v214, s12, v235
	v_fma_f32 v243, v215, s12, v235
	v_mfma_f32_32x32x16_bf16 v[2:17], v[118:121], v[138:141], v[2:17]
	v_exp_f32_e32 v220, v83
	v_exp_f32_e32 v221, v87
	v_exp_f32_e32 v222, v91
	v_exp_f32_e32 v223, v95
	v_fmac_f32_e32 v236, v216, v236
	v_fmac_f32_e32 v237, v217, v237
	v_fmac_f32_e32 v238, v218, v238
	v_fmac_f32_e32 v239, v219, v239
	v_mfma_f32_32x32x16_bf16 v[2:17], v[114:117], v[142:145], v[2:17]
	v_rcp_f32_e32 v216, v236
	v_rcp_f32_e32 v217, v237
	v_rcp_f32_e32 v218, v238
	v_rcp_f32_e32 v219, v239
	v_add_f32_e32 v220, 1.0, v220
	v_add_f32_e32 v221, 1.0, v221
	v_add_f32_e32 v222, 1.0, v222
	v_add_f32_e32 v223, 1.0, v223
	v_mfma_f32_32x32x16_bf16 v[2:17], v[110:113], v[146:149], v[2:17]
	v_rcp_f32_e32 v220, v220
	v_rcp_f32_e32 v221, v221
	v_rcp_f32_e32 v222, v222
	v_rcp_f32_e32 v223, v223
	v_mul_f32_e32 v240, v240, v216
	v_mul_f32_e32 v241, v241, v217
	v_mul_f32_e32 v242, v242, v218
	v_mul_f32_e32 v243, v243, v219
	v_mfma_f32_32x32x16_bf16 v[2:17], v[106:109], v[150:153], v[2:17]
	v_exp_f32_e32 v224, v85
	v_exp_f32_e32 v225, v89
	v_exp_f32_e32 v226, v93
	v_exp_f32_e32 v227, v97
	v_fma_f32 v206, v220, v206, v240
	v_fma_f32 v207, v221, v207, v241
	v_fma_f32 v208, v222, v208, v242
	v_fma_f32 v209, v223, v209, v243
	v_mfma_f32_32x32x16_bf16 v[2:17], v[102:105], v[154:157], v[2:17]
	v_exp_f32_e32 v212, v206
	v_exp_f32_e32 v213, v207
	v_exp_f32_e32 v214, v208
	v_exp_f32_e32 v215, v209
	v_add_f32_e32 v224, 1.0, v224
	v_add_f32_e32 v225, 1.0, v225
	v_add_f32_e32 v226, 1.0, v226
	v_add_f32_e32 v227, 1.0, v227
	v_fmac_f32_e32 v224, v224, v212
	v_fmac_f32_e32 v225, v225, v213
	v_fmac_f32_e32 v226, v226, v214
	v_fmac_f32_e32 v227, v227, v215
	v_mfma_f32_32x32x16_bf16 v[2:17], v[98:101], v[158:161], v[2:17]
	v_rcp_f32_e32 v224, v224
	v_rcp_f32_e32 v225, v225
	v_rcp_f32_e32 v226, v226
	v_rcp_f32_e32 v227, v227
	v_fma_f32 v224, -v212, v224, v224
	v_fma_f32 v225, -v213, v225, v225
	v_fma_f32 v226, -v214, v226, v226
	v_fma_f32 v227, -v215, v227, v227
	v_cvt_pk_bf16_f32 v224, v224, v225
	v_cvt_pk_bf16_f32 v225, v226, v227
	ds_write_b64 v211, v[224:225] offset:8200
	s_waitcnt lgkmcnt(0)
	s_barrier
	s_sub_u32 s16, s16, 1
	s_cmp_lg_u32 s16, 0
	s_cbranch_scc1 .Llight_loop
	v_mfma_f32_32x32x16_bf16 v[18:33], v[78:81], v[130:133], v[18:33]
	ds_read_b128 v[162:165], v210 offset:8192
	ds_read_b128 v[166:169], v210 offset:9216
	ds_read_b128 v[82:85], v234 offset:128
	ds_read_b128 v[86:89], v234 offset:144
	ds_read_b128 v[90:93], v234 offset:160
	ds_read_b128 v[94:97], v234 offset:176
	v_exp_f32_e32 v212, v4
	v_exp_f32_e32 v213, v8
	v_exp_f32_e32 v214, v12
	v_exp_f32_e32 v215, v16
	v_mfma_f32_32x32x16_bf16 v[18:33], v[74:77], v[134:137], v[18:33]
	ds_read_b128 v[170:173], v210 offset:10240
	ds_read_b128 v[174:177], v210 offset:11264
	v_exp_f32_e32 v216, v2
	v_exp_f32_e32 v217, v6
	v_exp_f32_e32 v218, v10
	v_exp_f32_e32 v219, v14
	v_add_f32_e32 v236, 1.0, v212
	v_add_f32_e32 v237, 1.0, v213
	v_add_f32_e32 v238, 1.0, v214
	v_add_f32_e32 v239, 1.0, v215
	v_fma_f32 v240, v212, s12, v235
	v_fma_f32 v241, v213, s12, v235
	v_fma_f32 v242, v214, s12, v235
	v_fma_f32 v243, v215, s12, v235
	v_mfma_f32_32x32x16_bf16 v[18:33], v[70:73], v[138:141], v[18:33]
	ds_read_b128 v[178:181], v210 offset:12288
	ds_read_b128 v[182:185], v210 offset:13312
	v_exp_f32_e32 v220, v3
	v_exp_f32_e32 v221, v7
	v_exp_f32_e32 v222, v11
	v_exp_f32_e32 v223, v15
	v_fmac_f32_e32 v236, v216, v236
	v_fmac_f32_e32 v237, v217, v237
	v_fmac_f32_e32 v238, v218, v238
	v_fmac_f32_e32 v239, v219, v239
	v_mfma_f32_32x32x16_bf16 v[18:33], v[66:69], v[142:145], v[18:33]
	ds_read_b128 v[186:189], v210 offset:14336
	ds_read_b128 v[190:193], v210 offset:15360
	v_rcp_f32_e32 v216, v236
	v_rcp_f32_e32 v217, v237
	v_rcp_f32_e32 v218, v238
	v_rcp_f32_e32 v219, v239
	v_add_f32_e32 v220, 1.0, v220
	v_add_f32_e32 v221, 1.0, v221
	v_add_f32_e32 v222, 1.0, v222
	v_add_f32_e32 v223, 1.0, v223
	v_mfma_f32_32x32x16_bf16 v[18:33], v[62:65], v[146:149], v[18:33]
	v_rcp_f32_e32 v220, v220
	v_rcp_f32_e32 v221, v221
	v_rcp_f32_e32 v222, v222
	v_rcp_f32_e32 v223, v223
	v_mul_f32_e32 v240, v240, v216
	v_mul_f32_e32 v241, v241, v217
	v_mul_f32_e32 v242, v242, v218
	v_mul_f32_e32 v243, v243, v219
	v_mfma_f32_32x32x16_bf16 v[18:33], v[58:61], v[150:153], v[18:33]
	v_exp_f32_e32 v224, v5
	v_exp_f32_e32 v225, v9
	v_exp_f32_e32 v226, v13
	v_exp_f32_e32 v227, v17
	v_fma_f32 v194, v220, v194, v240
	v_fma_f32 v195, v221, v195, v241
	v_fma_f32 v196, v222, v196, v242
	v_fma_f32 v197, v223, v197, v243
	v_mfma_f32_32x32x16_bf16 v[18:33], v[54:57], v[154:157], v[18:33]
	v_exp_f32_e32 v212, v194
	v_exp_f32_e32 v213, v195
	v_exp_f32_e32 v214, v196
	v_exp_f32_e32 v215, v197
	v_add_f32_e32 v224, 1.0, v224
	v_add_f32_e32 v225, 1.0, v225
	v_add_f32_e32 v226, 1.0, v226
	v_add_f32_e32 v227, 1.0, v227
	v_fmac_f32_e32 v224, v224, v212
	v_fmac_f32_e32 v225, v225, v213
	v_fmac_f32_e32 v226, v226, v214
	v_fmac_f32_e32 v227, v227, v215
	v_mfma_f32_32x32x16_bf16 v[18:33], v[50:53], v[158:161], v[18:33]
	v_rcp_f32_e32 v224, v224
	v_rcp_f32_e32 v225, v225
	v_rcp_f32_e32 v226, v226
	v_rcp_f32_e32 v227, v227
	v_fma_f32 v224, -v212, v224, v224
	v_fma_f32 v225, -v213, v225, v225
	v_fma_f32 v226, -v214, v226, v226
	v_fma_f32 v227, -v215, v227, v227
	v_cvt_pk_bf16_f32 v224, v224, v225
	v_cvt_pk_bf16_f32 v225, v226, v227
	ds_write_b64 v211, v[224:225] offset:0
	s_waitcnt lgkmcnt(1)
	v_mfma_f32_32x32x16_bf16 v[34:49], v[126:129], v[162:165], v[34:49]
	v_exp_f32_e32 v212, v20
	v_exp_f32_e32 v213, v24
	v_exp_f32_e32 v214, v28
	v_exp_f32_e32 v215, v32
	v_mfma_f32_32x32x16_bf16 v[34:49], v[122:125], v[166:169], v[34:49]
	v_exp_f32_e32 v216, v18
	v_exp_f32_e32 v217, v22
	v_exp_f32_e32 v218, v26
	v_exp_f32_e32 v219, v30
	v_add_f32_e32 v236, 1.0, v212
	v_add_f32_e32 v237, 1.0, v213
	v_add_f32_e32 v238, 1.0, v214
	v_add_f32_e32 v239, 1.0, v215
	v_fma_f32 v240, v212, s12, v235
	v_fma_f32 v241, v213, s12, v235
	v_fma_f32 v242, v214, s12, v235
	v_fma_f32 v243, v215, s12, v235
	v_mfma_f32_32x32x16_bf16 v[34:49], v[118:121], v[170:173], v[34:49]
	v_exp_f32_e32 v220, v19
	v_exp_f32_e32 v221, v23
	v_exp_f32_e32 v222, v27
	v_exp_f32_e32 v223, v31
	v_fmac_f32_e32 v236, v216, v236
	v_fmac_f32_e32 v237, v217, v237
	v_fmac_f32_e32 v238, v218, v238
	v_fmac_f32_e32 v239, v219, v239
	v_mfma_f32_32x32x16_bf16 v[34:49], v[114:117], v[174:177], v[34:49]
	v_rcp_f32_e32 v216, v236
	v_rcp_f32_e32 v217, v237
	v_rcp_f32_e32 v218, v238
	v_rcp_f32_e32 v219, v239
	v_add_f32_e32 v220, 1.0, v220
	v_add_f32_e32 v221, 1.0, v221
	v_add_f32_e32 v222, 1.0, v222
	v_add_f32_e32 v223, 1.0, v223
	v_mfma_f32_32x32x16_bf16 v[34:49], v[110:113], v[178:181], v[34:49]
	v_rcp_f32_e32 v220, v220
	v_rcp_f32_e32 v221, v221
	v_rcp_f32_e32 v222, v222
	v_rcp_f32_e32 v223, v223
	v_mul_f32_e32 v240, v240, v216
	v_mul_f32_e32 v241, v241, v217
	v_mul_f32_e32 v242, v242, v218
	v_mul_f32_e32 v243, v243, v219
	v_mfma_f32_32x32x16_bf16 v[34:49], v[106:109], v[182:185], v[34:49]
	v_exp_f32_e32 v224, v21
	v_exp_f32_e32 v225, v25
	v_exp_f32_e32 v226, v29
	v_exp_f32_e32 v227, v33
	v_fma_f32 v198, v220, v198, v240
	v_fma_f32 v199, v221, v199, v241
	v_fma_f32 v200, v222, v200, v242
	v_fma_f32 v201, v223, v201, v243
	v_mfma_f32_32x32x16_bf16 v[34:49], v[102:105], v[186:189], v[34:49]
	v_exp_f32_e32 v212, v198
	v_exp_f32_e32 v213, v199
	v_exp_f32_e32 v214, v200
	v_exp_f32_e32 v215, v201
	v_add_f32_e32 v224, 1.0, v224
	v_add_f32_e32 v225, 1.0, v225
	v_add_f32_e32 v226, 1.0, v226
	v_add_f32_e32 v227, 1.0, v227
	v_fmac_f32_e32 v224, v224, v212
	v_fmac_f32_e32 v225, v225, v213
	v_fmac_f32_e32 v226, v226, v214
	v_fmac_f32_e32 v227, v227, v215
	v_mfma_f32_32x32x16_bf16 v[34:49], v[98:101], v[190:193], v[34:49]
	v_rcp_f32_e32 v224, v224
	v_rcp_f32_e32 v225, v225
	v_rcp_f32_e32 v226, v226
	v_rcp_f32_e32 v227, v227
	v_fma_f32 v224, -v212, v224, v224
	v_fma_f32 v225, -v213, v225, v225
	v_fma_f32 v226, -v214, v226, v226
	v_fma_f32 v227, -v215, v227, v227
	v_cvt_pk_bf16_f32 v224, v224, v225
	v_cvt_pk_bf16_f32 v225, v226, v227
	ds_write_b64 v211, v[224:225] offset:8
	s_waitcnt lgkmcnt(0)
	s_barrier
	s_bfe_u32 s20, s19, 0x10006
	s_lshl_b32 s21, s20, 7
	s_lshl_b32 s20, s20, 13
	s_add_u32 s20, s20, 0x30000
	s_add_u32 s22, s14, s20
	s_addc_u32 s23, s15, 0
	s_add_u32 s24, s22, 0x1000
	s_addc_u32 s25, s23, 0
	global_load_dwordx4 v[130:133], v210, s[22:23] offset:0
	global_load_dwordx4 v[130:133], v210, s[22:23] offset:1024
	global_load_dwordx4 v[130:133], v210, s[22:23] offset:2048
	global_load_dwordx4 v[130:133], v210, s[22:23] offset:3072
	global_load_dwordx4 v[130:133], v210, s[24:25] offset:0
	global_load_dwordx4 v[130:133], v210, s[24:25] offset:1024
	global_load_dwordx4 v[130:133], v210, s[24:25] offset:2048
	global_load_dwordx4 v[130:133], v210, s[24:25] offset:3072
	v_or_b32_e32 v138, s21, v230
	global_load_dwordx4 v[134:137], v138, s[4:5] offset:0
	global_load_dwordx4 v[134:137], v138, s[4:5] offset:32
	global_load_dwordx4 v[134:137], v138, s[4:5] offset:64
	global_load_dwordx4 v[134:137], v138, s[4:5] offset:96
	global_load_dwordx4 v[134:137], v138, s[6:7] offset:0
	global_load_dwordx4 v[134:137], v138, s[6:7] offset:32
	global_load_dwordx4 v[134:137], v138, s[6:7] offset:64
	global_load_dwordx4 v[134:137], v138, s[6:7] offset:96
	s_load_dword s21, s[8:9], 0x0
	v_mfma_f32_32x32x16_bf16 v[82:97], v[78:81], v[162:165], v[82:97]
	v_exp_f32_e32 v212, v36
	v_exp_f32_e32 v213, v40
	v_exp_f32_e32 v214, v44
	v_exp_f32_e32 v215, v48
	v_mfma_f32_32x32x16_bf16 v[82:97], v[74:77], v[166:169], v[82:97]
	v_exp_f32_e32 v216, v34
	v_exp_f32_e32 v217, v38
	v_exp_f32_e32 v218, v42
	v_exp_f32_e32 v219, v46
	v_add_f32_e32 v236, 1.0, v212
	v_add_f32_e32 v237, 1.0, v213
	v_add_f32_e32 v238, 1.0, v214
	v_add_f32_e32 v239, 1.0, v215
	v_fma_f32 v240, v212, s12, v235
	v_fma_f32 v241, v213, s12, v235
	v_fma_f32 v242, v214, s12, v235
	v_fma_f32 v243, v215, s12, v235
	v_mfma_f32_32x32x16_bf16 v[82:97], v[70:73], v[170:173], v[82:97]
	v_exp_f32_e32 v220, v35
	v_exp_f32_e32 v221, v39
	v_exp_f32_e32 v222, v43
	v_exp_f32_e32 v223, v47
	v_fmac_f32_e32 v236, v216, v236
	v_fmac_f32_e32 v237, v217, v237
	v_fmac_f32_e32 v238, v218, v238
	v_fmac_f32_e32 v239, v219, v239
	v_mfma_f32_32x32x16_bf16 v[82:97], v[66:69], v[174:177], v[82:97]
	v_rcp_f32_e32 v216, v236
	v_rcp_f32_e32 v217, v237
	v_rcp_f32_e32 v218, v238
	v_rcp_f32_e32 v219, v239
	v_add_f32_e32 v220, 1.0, v220
	v_add_f32_e32 v221, 1.0, v221
	v_add_f32_e32 v222, 1.0, v222
	v_add_f32_e32 v223, 1.0, v223
	v_mfma_f32_32x32x16_bf16 v[82:97], v[62:65], v[178:181], v[82:97]
	v_rcp_f32_e32 v220, v220
	v_rcp_f32_e32 v221, v221
	v_rcp_f32_e32 v222, v222
	v_rcp_f32_e32 v223, v223
	v_mul_f32_e32 v240, v240, v216
	v_mul_f32_e32 v241, v241, v217
	v_mul_f32_e32 v242, v242, v218
	v_mul_f32_e32 v243, v243, v219
	v_mfma_f32_32x32x16_bf16 v[82:97], v[58:61], v[182:185], v[82:97]
	v_exp_f32_e32 v224, v37
	v_exp_f32_e32 v225, v41
	v_exp_f32_e32 v226, v45
	v_exp_f32_e32 v227, v49
	v_fma_f32 v202, v220, v202, v240
	v_fma_f32 v203, v221, v203, v241
	v_fma_f32 v204, v222, v204, v242
	v_fma_f32 v205, v223, v205, v243
	v_mfma_f32_32x32x16_bf16 v[82:97], v[54:57], v[186:189], v[82:97]
	v_exp_f32_e32 v212, v202
	v_exp_f32_e32 v213, v203
	v_exp_f32_e32 v214, v204
	v_exp_f32_e32 v215, v205
	v_add_f32_e32 v224, 1.0, v224
	v_add_f32_e32 v225, 1.0, v225
	v_add_f32_e32 v226, 1.0, v226
	v_add_f32_e32 v227, 1.0, v227
	v_fmac_f32_e32 v224, v224, v212
	v_fmac_f32_e32 v225, v225, v213
	v_fmac_f32_e32 v226, v226, v214
	v_fmac_f32_e32 v227, v227, v215
	v_mfma_f32_32x32x16_bf16 v[82:97], v[50:53], v[190:193], v[82:97]
	v_rcp_f32_e32 v224, v224
	v_rcp_f32_e32 v225, v225
	v_rcp_f32_e32 v226, v226
	v_rcp_f32_e32 v227, v227
	v_fma_f32 v224, -v212, v224, v224
	v_fma_f32 v225, -v213, v225, v225
	v_fma_f32 v226, -v214, v226, v226
	v_fma_f32 v227, -v215, v227, v227
	v_cvt_pk_bf16_f32 v224, v224, v225
	v_cvt_pk_bf16_f32 v225, v226, v227
	ds_write_b64 v211, v[224:225] offset:8192
	s_waitcnt lgkmcnt(1)
	v_exp_f32_e32 v212, v84
	v_exp_f32_e32 v213, v88
	v_exp_f32_e32 v214, v92
	v_exp_f32_e32 v215, v96
	v_exp_f32_e32 v216, v82
	v_exp_f32_e32 v217, v86
	v_exp_f32_e32 v218, v90
	v_exp_f32_e32 v219, v94
	v_add_f32_e32 v236, 1.0, v212
	v_add_f32_e32 v237, 1.0, v213
	v_add_f32_e32 v238, 1.0, v214
	v_add_f32_e32 v239, 1.0, v215
	v_fma_f32 v240, v212, s12, v235
	v_fma_f32 v241, v213, s12, v235
	v_fma_f32 v242, v214, s12, v235
	v_fma_f32 v243, v215, s12, v235
	v_exp_f32_e32 v220, v83
	v_exp_f32_e32 v221, v87
	v_exp_f32_e32 v222, v91
	v_exp_f32_e32 v223, v95
	v_fmac_f32_e32 v236, v216, v236
	v_fmac_f32_e32 v237, v217, v237
	v_fmac_f32_e32 v238, v218, v238
	v_fmac_f32_e32 v239, v219, v239
	v_rcp_f32_e32 v216, v236
	v_rcp_f32_e32 v217, v237
	v_rcp_f32_e32 v218, v238
	v_rcp_f32_e32 v219, v239
	v_add_f32_e32 v220, 1.0, v220
	v_add_f32_e32 v221, 1.0, v221
	v_add_f32_e32 v222, 1.0, v222
	v_add_f32_e32 v223, 1.0, v223
	v_rcp_f32_e32 v220, v220
	v_rcp_f32_e32 v221, v221
	v_rcp_f32_e32 v222, v222
	v_rcp_f32_e32 v223, v223
	v_mul_f32_e32 v240, v240, v216
	v_mul_f32_e32 v241, v241, v217
	v_mul_f32_e32 v242, v242, v218
	v_mul_f32_e32 v243, v243, v219
	v_exp_f32_e32 v224, v85
	v_exp_f32_e32 v225, v89
	v_exp_f32_e32 v226, v93
	v_exp_f32_e32 v227, v97
	v_fma_f32 v206, v220, v206, v240
	v_fma_f32 v207, v221, v207, v241
	v_fma_f32 v208, v222, v208, v242
	v_fma_f32 v209, v223, v209, v243
	v_exp_f32_e32 v212, v206
	v_exp_f32_e32 v213, v207
	v_exp_f32_e32 v214, v208
	v_exp_f32_e32 v215, v209
	v_add_f32_e32 v224, 1.0, v224
	v_add_f32_e32 v225, 1.0, v225
	v_add_f32_e32 v226, 1.0, v226
	v_add_f32_e32 v227, 1.0, v227
	v_fmac_f32_e32 v224, v224, v212
	v_fmac_f32_e32 v225, v225, v213
	v_fmac_f32_e32 v226, v226, v214
	v_fmac_f32_e32 v227, v227, v215
	v_rcp_f32_e32 v224, v224
	v_rcp_f32_e32 v225, v225
	v_rcp_f32_e32 v226, v226
	v_rcp_f32_e32 v227, v227
	v_fma_f32 v224, -v212, v224, v224
	v_fma_f32 v225, -v213, v225, v225
	v_fma_f32 v226, -v214, v226, v226
	v_fma_f32 v227, -v215, v227, v227
	v_cvt_pk_bf16_f32 v224, v224, v225
	v_cvt_pk_bf16_f32 v225, v226, v227
	ds_write_b64 v211, v[224:225] offset:8200
	s_waitcnt lgkmcnt(0)
	s_barrier
	s_waitcnt vmcnt(0)
	s_nop 7
	s_nop 7
	s_branch .Lepilogue

	.amdhsa_kernel _Z11lstm_kernelPKiPKhPKfS4_S4_Pf
		.amdhsa_group_segment_fixed_size 163840
		.amdhsa_private_segment_fixed_size 0
		.amdhsa_kernarg_size 48
		.amdhsa_user_sgpr_count 2
		.amdhsa_user_sgpr_dispatch_ptr 0
		.amdhsa_user_sgpr_queue_ptr 0
		.amdhsa_user_sgpr_kernarg_segment_ptr 1
		.amdhsa_user_sgpr_dispatch_id 0
		.amdhsa_user_sgpr_kernarg_preload_length 0
		.amdhsa_user_sgpr_kernarg_preload_offset 0
		.amdhsa_user_sgpr_private_segment_size 0
		.amdhsa_uses_dynamic_stack 0
		.amdhsa_enable_private_segment 0
		.amdhsa_system_sgpr_workgroup_id_x 1
		.amdhsa_system_sgpr_workgroup_id_y 0
		.amdhsa_system_sgpr_workgroup_id_z 0
		.amdhsa_system_sgpr_workgroup_info 0
		.amdhsa_system_vgpr_workitem_id 0
		.amdhsa_next_free_vgpr 256
		.amdhsa_next_free_sgpr 91
		.amdhsa_accum_offset 256
		.amdhsa_reserve_vcc 1
		.amdhsa_float_round_mode_32 0
		.amdhsa_float_round_mode_16_64 0
		.amdhsa_float_denorm_mode_32 3
		.amdhsa_float_denorm_mode_16_64 3
		.amdhsa_dx10_clamp 1
		.amdhsa_ieee_mode 1
		.amdhsa_fp16_overflow 0
		.amdhsa_tg_split 0
		.amdhsa_exception_fp_ieee_invalid_op 0
		.amdhsa_exception_fp_denorm_src 0
		.amdhsa_exception_fp_ieee_div_zero 0
		.amdhsa_exception_fp_ieee_overflow 0
		.amdhsa_exception_fp_ieee_underflow 0
		.amdhsa_exception_fp_ieee_inexact 0
		.amdhsa_exception_int_div_zero 0
	.end_amdhsa_kernel

amdhsa.kernels:
  - .agpr_count:     0
    .args:
      - .actual_access:  read_only
        .address_space:  global
        .offset:         0
        .size:           8
        .value_kind:     global_buffer
      - .actual_access:  read_only
        .address_space:  global
        .offset:         8
        .size:           8
        .value_kind:     global_buffer
      - .actual_access:  read_only
        .address_space:  global
        .offset:         16
        .size:           8
        .value_kind:     global_buffer
      - .actual_access:  read_only
        .address_space:  global
        .offset:         24
        .size:           8
        .value_kind:     global_buffer
      - .actual_access:  read_only
        .address_space:  global
        .offset:         32
        .size:           8
        .value_kind:     global_buffer
      - .actual_access:  read_only
        .address_space:  global
        .offset:         40
        .size:           8
        .value_kind:     global_buffer
      - .actual_access:  write_only
        .address_space:  global
        .offset:         48
        .size:           8
        .value_kind:     global_buffer
      - .offset:         56
        .size:           4
        .value_kind:     hidden_block_count_x
      - .offset:         60
        .size:           4
        .value_kind:     hidden_block_count_y
      - .offset:         64
        .size:           4
        .value_kind:     hidden_block_count_z
      - .offset:         68
        .size:           2
        .value_kind:     hidden_group_size_x
      - .offset:         70
        .size:           2
        .value_kind:     hidden_group_size_y
      - .offset:         72
        .size:           2
        .value_kind:     hidden_group_size_z
      - .offset:         74
        .size:           2
        .value_kind:     hidden_remainder_x
      - .offset:         76
        .size:           2
        .value_kind:     hidden_remainder_y
      - .offset:         78
        .size:           2
        .value_kind:     hidden_remainder_z
      - .offset:         96
        .size:           8
        .value_kind:     hidden_global_offset_x
      - .offset:         104
        .size:           8
        .value_kind:     hidden_global_offset_y
      - .offset:         112
        .size:           8
        .value_kind:     hidden_global_offset_z
      - .offset:         120
        .size:           2
        .value_kind:     hidden_grid_dims
    .group_segment_fixed_size: 0
    .kernarg_segment_align: 8
    .kernarg_segment_size: 312
    .language:       OpenCL C
    .language_version:
      - 2
      - 0
    .max_flat_workgroup_size: 1024
    .name:           _Z11prep_kernelPKfS0_S0_S0_S0_S0_Ph
    .private_segment_fixed_size: 0
    .sgpr_count:     22
    .sgpr_spill_count: 0
    .symbol:         _Z11prep_kernelPKfS0_S0_S0_S0_S0_Ph.kd
    .uniform_work_group_size: 1
    .uses_dynamic_stack: false
    .vgpr_count:     20
    .vgpr_spill_count: 0
    .wavefront_size: 64
  - .agpr_count:     0
    .args:
      - .actual_access:  read_only
        .address_space:  global
        .offset:         0
        .size:           8
        .value_kind:     global_buffer
      - .actual_access:  read_only
        .address_space:  global
        .offset:         8
        .size:           8
        .value_kind:     global_buffer
      - .actual_access:  read_only
        .address_space:  global
        .offset:         16
        .size:           8
        .value_kind:     global_buffer
      - .actual_access:  read_only
        .address_space:  global
        .offset:         24
        .size:           8
        .value_kind:     global_buffer
      - .actual_access:  read_only
        .address_space:  global
        .offset:         32
        .size:           8
        .value_kind:     global_buffer
      - .actual_access:  write_only
        .address_space:  global
        .offset:         40
        .size:           8
        .value_kind:     global_buffer
    .group_segment_fixed_size: 163840
    .kernarg_segment_align: 8
    .kernarg_segment_size: 48
    .language:       OpenCL C
    .language_version:
      - 2
      - 0
    .max_flat_workgroup_size: 512
    .name:           _Z11lstm_kernelPKiPKhPKfS4_S4_Pf
    .private_segment_fixed_size: 0
    .sgpr_count:     26
    .sgpr_spill_count: 0
    .symbol:         _Z11lstm_kernelPKiPKhPKfS4_S4_Pf.kd
    .uniform_work_group_size: 1
    .uses_dynamic_stack: false
    .vgpr_count:     256
    .vgpr_spill_count: 0
    .wavefront_size: 64
